# residual GEMM epilogues (out-projections, FFN-down): counted wait in front of each 8-value group instead of one vmcnt(0) behind the sixteen residual loads
# speedup vs baseline: 1.0015x; 1.0015x over previous
; __device__ __forceinline__ void st16_wt(void* p, u32x4 v) { asm volatile("global_store_dwordx4 %0, %1, off sc1\n\ts_nop 1" :: "v"(p), "v"(v) : "memory"); }
; __device__ __forceinline__ unsigned cvt_pk_bf16(float lo, float hi) { unsigned r; asm volatile("v_cvt_pk_bf16_f32 %0, %1, %2" : "=v"(r) : "v"(lo), "v"(hi)); return r; }
;     __device__ __forceinline__ void operator()(const Acc& acc, const Unit& u, int wr, int wc, int fr, int fq, const LAS float* tab) const {
;     ...
;                     for (int bj = 0; bj < 2; ++bj) rb[ai][m][bj] = *(const u32x4*)(xb + ((size_t)u.pm * BM + ai * HALF + wr * 64 + m * 16 + fr) * D + col0 + bj * HALF);
;     ...
;                 const size_t row = (size_t)u.pm * BM + ai * HALF + wr * 64 + m * 16 + fr; const size_t off = row * D + col0; float ss = 0.f;
; #pragma unroll
;                 for (int bj = 0; bj < 2; ++bj) { f32x4 b0, b1;
;                     if (base32) { b0 = __builtin_nontemporal_load((const f32x4*)(base32 + off + bj * HALF)); b1 = __builtin_nontemporal_load((const f32x4*)(base32 + off + bj * HALF + 4)); }
;                     else { const u32x4 b4 = rb[ai][m][bj];
;                         b0 = (f32x4){__uint_as_float(b4.x << 16), __uint_as_float(b4.x & 0xFFFF0000u), __uint_as_float(b4.y << 16), __uint_as_float(b4.y & 0xFFFF0000u)};
;                         b1 = (f32x4){__uint_as_float(b4.z << 16), __uint_as_float(b4.z & 0xFFFF0000u), __uint_as_float(b4.w << 16), __uint_as_float(b4.w & 0xFFFF0000u)}; }
;                     const f32x4 o0 = b0 + acc[ai][bj][m][0], o1 = b1 + acc[ai][bj][m][1];
;                     if (out32) {
;                         if (!dry) { *(f32x4*)(out32 + off + bj * HALF) = o0; *(f32x4*)(out32 + off + bj * HALF + 4) = o1; }
;                         continue; }
;                     ss += ((o0[0] * o0[0] + o0[1] * o0[1]) + (o0[2] * o0[2] + o0[3] * o0[3])) + ((o1[0] * o1[0] + o1[1] * o1[1]) + (o1[2] * o1[2] + o1[3] * o1[3]));
;                     u32x4 w; w.x = cvt_pk_bf16(o0[0], o0[1]); w.y = cvt_pk_bf16(o0[2], o0[3]); w.z = cvt_pk_bf16(o1[0], o1[1]); w.w = cvt_pk_bf16(o1[2], o1[3]);
;                     if (!dry) st16_wt(xb + off + bj * HALF, w); }
;                 if (out32) continue;
;                 ss = sum_rows4(ss);
;                 if (fq == 0 && !dry) ssp[row * 16 + u.pn * 4 + wc] = ss;
.LBB0_438:
	v_lshl_or_b32 v206, s22, 8, v213
	s_ashr_i32 s25, s24, 31
	s_lshl_b64 s[0:1], s[24:25], 8
	v_ashrrev_i32_e32 v207, 31, v206
	v_lshl_add_u64 v[208:209], s[0:1], 0, v[196:197]
	v_lshlrev_b64 v[210:211], 1, v[206:207]
	v_lshl_add_u64 v[98:99], s[10:11], 0, v[210:211]
	v_lshlrev_b64 v[220:221], 11, v[208:209]
	v_lshl_add_u64 v[98:99], v[98:99], 0, v[220:221]
	v_add_co_u32_e32 v100, vcc, 0x8000, v98
	global_load_dwordx4 v[216:219], v[98:99], off
	global_load_dwordx4 v[186:189], v[98:99], off offset:256
	v_addc_co_u32_e32 v101, vcc, 0, v99, vcc
	global_load_dwordx4 v[182:185], v[100:101], off
	global_load_dwordx4 v[178:181], v[100:101], off offset:256
	v_add_co_u32_e32 v100, vcc, 0x10000, v98
	v_lshl_add_u64 v[220:221], s[10:11], 0, v[220:221]
	s_nop 0
	v_addc_co_u32_e32 v101, vcc, 0, v99, vcc
	global_load_dwordx4 v[174:177], v[100:101], off
	global_load_dwordx4 v[170:173], v[100:101], off offset:256
	v_add_co_u32_e32 v100, vcc, 0x18000, v98
	v_lshl_add_u64 v[210:211], v[220:221], 0, v[210:211]
	s_nop 0
	v_addc_co_u32_e32 v101, vcc, 0, v99, vcc
	global_load_dwordx4 v[166:169], v[100:101], off
	global_load_dwordx4 v[162:165], v[100:101], off offset:256
	v_add_co_u32_e32 v100, vcc, 0x40000, v98
	s_lshl_b32 s0, s22, 2
	s_nop 0
	v_addc_co_u32_e32 v101, vcc, 0, v99, vcc
	global_load_dwordx4 v[158:161], v[100:101], off
	global_load_dwordx4 v[146:149], v[100:101], off offset:256
	v_add_co_u32_e32 v100, vcc, 0x48000, v98
	s_ashr_i32 s1, s0, 31
	s_nop 0
	v_addc_co_u32_e32 v101, vcc, 0, v99, vcc
	global_load_dwordx4 v[142:145], v[100:101], off
	global_load_dwordx4 v[138:141], v[100:101], off offset:256
	v_add_co_u32_e32 v100, vcc, 0x50000, v98
	s_lshl_b64 s[0:1], s[0:1], 2
	s_nop 0
	v_addc_co_u32_e32 v101, vcc, 0, v99, vcc
	v_add_co_u32_e32 v98, vcc, 0x58000, v98
	global_load_dwordx4 v[134:137], v[100:101], off
	global_load_dwordx4 v[122:125], v[100:101], off offset:256
	v_addc_co_u32_e32 v99, vcc, 0, v99, vcc
	global_load_dwordx4 v[110:113], v[98:99], off
	s_nop 0
	global_load_dwordx4 v[98:101], v[98:99], off offset:256
	s_add_u32 s22, s46, s0
	s_addc_u32 s23, s47, s1
	s_mov_b64 s[0:1], 0x100
	s_nop 0
	s_waitcnt vmcnt(15)
	v_lshlrev_b32_e32 v220, 16, v216
	v_and_b32_e32 v221, 0xffff0000, v216
	v_lshlrev_b32_e32 v216, 16, v217
	v_and_b32_e32 v217, 0xffff0000, v217
	v_lshlrev_b32_e32 v222, 16, v218
	v_and_b32_e32 v223, 0xffff0000, v218
	v_lshlrev_b32_e32 v218, 16, v219
	v_and_b32_e32 v219, 0xffff0000, v219
	v_pk_add_f32 v[156:157], v[156:157], v[216:217]
	v_pk_add_f32 v[154:155], v[154:155], v[220:221]
	v_pk_add_f32 v[216:217], v[152:153], v[218:219]
	v_pk_add_f32 v[152:153], v[150:151], v[222:223]
	v_mul_f32_e32 v150, v155, v155
	v_mul_f32_e32 v151, v157, v157
	v_fmac_f32_e32 v150, v154, v154
	v_fmac_f32_e32 v151, v156, v156
	v_add_f32_e32 v150, v150, v151
	v_mul_f32_e32 v151, v153, v153
	v_mul_f32_e32 v215, v217, v217
	v_fmac_f32_e32 v151, v152, v152
	v_fmac_f32_e32 v215, v216, v216
	v_add_f32_e32 v151, v151, v215
	v_add_f32_e32 v215, v150, v151
	v_cvt_pk_bf16_f32 v150, v154, v155
	v_cvt_pk_bf16_f32 v151, v156, v157
	v_cvt_pk_bf16_f32 v152, v152, v153
	v_cvt_pk_bf16_f32 v153, v216, v217
	s_waitcnt vmcnt(14)
	v_lshlrev_b32_e32 v154, 16, v188
	global_store_dwordx4 v[210:211], v[150:153], off sc1
	s_nop 1
	v_lshlrev_b32_e32 v150, 16, v186
	v_and_b32_e32 v151, 0xffff0000, v186
	v_lshlrev_b32_e32 v152, 16, v187
	v_and_b32_e32 v153, 0xffff0000, v187
	v_and_b32_e32 v155, 0xffff0000, v188
	v_lshlrev_b32_e32 v156, 16, v189
	v_and_b32_e32 v157, 0xffff0000, v189
	v_pk_add_f32 v[132:133], v[132:133], v[152:153]
	v_pk_add_f32 v[130:131], v[130:131], v[150:151]
	v_pk_add_f32 v[150:151], v[128:129], v[156:157]
	v_pk_add_f32 v[128:129], v[126:127], v[154:155]
	v_mul_f32_e32 v126, v131, v131
	v_mul_f32_e32 v127, v133, v133
	v_fmac_f32_e32 v126, v130, v130
	v_fmac_f32_e32 v127, v132, v132
	v_add_f32_e32 v126, v126, v127
	v_mul_f32_e32 v127, v129, v129
	v_mul_f32_e32 v152, v151, v151
	v_fmac_f32_e32 v127, v128, v128
	v_fmac_f32_e32 v152, v150, v150
	v_add_f32_e32 v127, v127, v152
	v_add_f32_e32 v126, v126, v127
	v_add_f32_e32 v152, v215, v126
	v_cvt_pk_bf16_f32 v126, v130, v131
	v_cvt_pk_bf16_f32 v127, v132, v133
	v_cvt_pk_bf16_f32 v128, v128, v129
	v_cvt_pk_bf16_f32 v129, v150, v151
	v_lshl_add_u64 v[130:131], v[210:211], 0, s[0:1]
	global_store_dwordx4 v[130:131], v[126:129], off sc1
	s_nop 1
	v_mov_b32_e32 v126, v152
	s_nop 1
	v_permlane16_swap_b32_e32 v152, v126
	v_add_f32_e32 v126, v152, v126
	v_mov_b32_e32 v127, v126
	s_nop 1
	v_permlane32_swap_b32_e32 v126, v127
	s_and_saveexec_b64 s[24:25], s[4:5]
	s_cbranch_execz .LBB0_440
	v_add_f32_e32 v128, v126, v127
	v_lshlrev_b64 v[126:127], 6, v[208:209]
	v_lshl_add_u64 v[126:127], s[22:23], 0, v[126:127]
	global_store_dword v[126:127], v128, off
; __device__ __forceinline__ void st16_wt(void* p, u32x4 v) { asm volatile("global_store_dwordx4 %0, %1, off sc1\n\ts_nop 1" :: "v"(p), "v"(v) : "memory"); }
; __device__ __forceinline__ unsigned cvt_pk_bf16(float lo, float hi) { unsigned r; asm volatile("v_cvt_pk_bf16_f32 %0, %1, %2" : "=v"(r) : "v"(lo), "v"(hi)); return r; }
;     __device__ __forceinline__ void operator()(const Acc& acc, const Unit& u, int wr, int wc, int fr, int fq, const LAS float* tab) const {
;     ...
;                 const size_t row = (size_t)u.pm * BM + ai * HALF + wr * 64 + m * 16 + fr; const size_t off = row * D + col0; float ss = 0.f;
; #pragma unroll
;                 for (int bj = 0; bj < 2; ++bj) { f32x4 b0, b1;
;                     if (base32) { b0 = __builtin_nontemporal_load((const f32x4*)(base32 + off + bj * HALF)); b1 = __builtin_nontemporal_load((const f32x4*)(base32 + off + bj * HALF + 4)); }
;                     else { const u32x4 b4 = rb[ai][m][bj];
;                         b0 = (f32x4){__uint_as_float(b4.x << 16), __uint_as_float(b4.x & 0xFFFF0000u), __uint_as_float(b4.y << 16), __uint_as_float(b4.y & 0xFFFF0000u)};
;                         b1 = (f32x4){__uint_as_float(b4.z << 16), __uint_as_float(b4.z & 0xFFFF0000u), __uint_as_float(b4.w << 16), __uint_as_float(b4.w & 0xFFFF0000u)}; }
;                     const f32x4 o0 = b0 + acc[ai][bj][m][0], o1 = b1 + acc[ai][bj][m][1];
;                     if (out32) {
;                         if (!dry) { *(f32x4*)(out32 + off + bj * HALF) = o0; *(f32x4*)(out32 + off + bj * HALF + 4) = o1; }
;                         continue; }
;                     ss += ((o0[0] * o0[0] + o0[1] * o0[1]) + (o0[2] * o0[2] + o0[3] * o0[3])) + ((o1[0] * o1[0] + o1[1] * o1[1]) + (o1[2] * o1[2] + o1[3] * o1[3]));
;                     u32x4 w; w.x = cvt_pk_bf16(o0[0], o0[1]); w.y = cvt_pk_bf16(o0[2], o0[3]); w.z = cvt_pk_bf16(o1[0], o1[1]); w.w = cvt_pk_bf16(o1[2], o1[3]);
;                     if (!dry) st16_wt(xb + off + bj * HALF, w); }
;                 if (out32) continue;
;                 ss = sum_rows4(ss);
;                 if (fq == 0 && !dry) ssp[row * 16 + u.pn * 4 + wc] = ss;
.LBB0_440:
	s_or_b64 exec, exec, s[24:25]
	s_waitcnt vmcnt(13)
	v_lshlrev_b32_e32 v130, 16, v182
	v_and_b32_e32 v131, 0xffff0000, v182
	v_lshlrev_b32_e32 v132, 16, v183
	v_and_b32_e32 v133, 0xffff0000, v183
	v_lshlrev_b32_e32 v150, 16, v184
	v_and_b32_e32 v151, 0xffff0000, v184
	v_lshlrev_b32_e32 v152, 16, v185
	v_and_b32_e32 v153, 0xffff0000, v185
	v_pk_add_f32 v[120:121], v[120:121], v[132:133]
	v_pk_add_f32 v[118:119], v[118:119], v[130:131]
	v_pk_add_f32 v[130:131], v[116:117], v[152:153]
	v_pk_add_f32 v[116:117], v[114:115], v[150:151]
	v_mul_f32_e32 v114, v119, v119
	v_mul_f32_e32 v115, v121, v121
	v_fmac_f32_e32 v114, v118, v118
	v_fmac_f32_e32 v115, v120, v120
	v_add_f32_e32 v114, v114, v115
	v_mul_f32_e32 v115, v117, v117
	v_mul_f32_e32 v132, v131, v131
	v_or_b32_e32 v126, 16, v208
	v_mov_b32_e32 v127, v209
	v_fmac_f32_e32 v115, v116, v116
	v_fmac_f32_e32 v132, v130, v130
	v_lshlrev_b64 v[128:129], 11, v[126:127]
	v_add_f32_e32 v115, v115, v132
	v_lshl_add_u64 v[128:129], s[10:11], 0, v[128:129]
	v_add_f32_e32 v132, v114, v115
	v_cvt_pk_bf16_f32 v114, v118, v119
	v_cvt_pk_bf16_f32 v115, v120, v121
	v_cvt_pk_bf16_f32 v116, v116, v117
	v_cvt_pk_bf16_f32 v117, v130, v131
	v_lshl_add_u64 v[128:129], v[206:207], 1, v[128:129]
	global_store_dwordx4 v[128:129], v[114:117], off sc1
	s_nop 1
	s_waitcnt vmcnt(12)
	v_lshlrev_b32_e32 v114, 16, v178
	v_and_b32_e32 v115, 0xffff0000, v178
	v_lshlrev_b32_e32 v116, 16, v179
	v_and_b32_e32 v117, 0xffff0000, v179
	v_lshlrev_b32_e32 v118, 16, v180
	v_and_b32_e32 v119, 0xffff0000, v180
	v_lshlrev_b32_e32 v120, 16, v181
	v_and_b32_e32 v121, 0xffff0000, v181
	v_pk_add_f32 v[108:109], v[108:109], v[116:117]
	v_pk_add_f32 v[106:107], v[106:107], v[114:115]
	v_pk_add_f32 v[114:115], v[104:105], v[120:121]
	v_pk_add_f32 v[104:105], v[102:103], v[118:119]
	v_mul_f32_e32 v102, v107, v107
	v_mul_f32_e32 v103, v109, v109
	v_fmac_f32_e32 v102, v106, v106
	v_fmac_f32_e32 v103, v108, v108
	v_add_f32_e32 v102, v102, v103
	v_mul_f32_e32 v103, v105, v105
	v_mul_f32_e32 v116, v115, v115
	v_fmac_f32_e32 v103, v104, v104
	v_fmac_f32_e32 v116, v114, v114
	v_add_f32_e32 v103, v103, v116
	v_add_f32_e32 v102, v102, v103
	v_add_f32_e32 v116, v132, v102
	v_cvt_pk_bf16_f32 v102, v106, v107
	v_cvt_pk_bf16_f32 v103, v108, v109
	v_cvt_pk_bf16_f32 v104, v104, v105
	v_cvt_pk_bf16_f32 v105, v114, v115
	v_lshl_add_u64 v[106:107], v[128:129], 0, s[0:1]
	global_store_dwordx4 v[106:107], v[102:105], off sc1
	s_nop 1
	v_mov_b32_e32 v102, v116
	s_nop 1
	v_permlane16_swap_b32_e32 v116, v102
	v_add_f32_e32 v102, v116, v102
	v_mov_b32_e32 v103, v102
	s_nop 1
	v_permlane32_swap_b32_e32 v102, v103
	s_and_saveexec_b64 s[24:25], s[4:5]
	s_cbranch_execz .LBB0_442
	v_add_f32_e32 v104, v102, v103
	v_lshlrev_b64 v[102:103], 6, v[126:127]
	v_lshl_add_u64 v[102:103], s[22:23], 0, v[102:103]
	global_store_dword v[102:103], v104, off
.LBB0_442:
	s_or_b64 exec, exec, s[24:25]
	s_waitcnt vmcnt(11)
	v_lshlrev_b32_e32 v106, 16, v174
	v_and_b32_e32 v107, 0xffff0000, v174
	v_lshlrev_b32_e32 v108, 16, v175
	v_and_b32_e32 v109, 0xffff0000, v175
	v_lshlrev_b32_e32 v114, 16, v176
	v_and_b32_e32 v115, 0xffff0000, v176
	v_lshlrev_b32_e32 v116, 16, v177
	v_and_b32_e32 v117, 0xffff0000, v177
	v_pk_add_f32 v[96:97], v[96:97], v[108:109]
	v_pk_add_f32 v[94:95], v[94:95], v[106:107]
	v_pk_add_f32 v[106:107], v[92:93], v[116:117]
	v_pk_add_f32 v[92:93], v[90:91], v[114:115]
	v_mul_f32_e32 v90, v95, v95
	v_mul_f32_e32 v91, v97, v97
	v_fmac_f32_e32 v90, v94, v94
	v_fmac_f32_e32 v91, v96, v96
	v_add_f32_e32 v90, v90, v91
	v_mul_f32_e32 v91, v93, v93
	v_mul_f32_e32 v108, v107, v107
	v_or_b32_e32 v102, 32, v208
	v_mov_b32_e32 v103, v209
	v_fmac_f32_e32 v91, v92, v92
	v_fmac_f32_e32 v108, v106, v106
	v_lshlrev_b64 v[104:105], 11, v[102:103]
	v_add_f32_e32 v91, v91, v108
	v_lshl_add_u64 v[104:105], s[10:11], 0, v[104:105]
	v_add_f32_e32 v108, v90, v91
	v_cvt_pk_bf16_f32 v90, v94, v95
	v_cvt_pk_bf16_f32 v91, v96, v97
	v_cvt_pk_bf16_f32 v92, v92, v93
	v_cvt_pk_bf16_f32 v93, v106, v107
	v_lshl_add_u64 v[104:105], v[206:207], 1, v[104:105]
	global_store_dwordx4 v[104:105], v[90:93], off sc1
	s_nop 1
	s_waitcnt vmcnt(10)
	v_lshlrev_b32_e32 v90, 16, v170
	v_and_b32_e32 v91, 0xffff0000, v170
	v_lshlrev_b32_e32 v92, 16, v171
	v_and_b32_e32 v93, 0xffff0000, v171
	v_lshlrev_b32_e32 v94, 16, v172
	v_and_b32_e32 v95, 0xffff0000, v172
	v_lshlrev_b32_e32 v96, 16, v173
	v_and_b32_e32 v97, 0xffff0000, v173
	v_pk_add_f32 v[88:89], v[88:89], v[92:93]
	v_pk_add_f32 v[86:87], v[86:87], v[90:91]
	v_pk_add_f32 v[90:91], v[84:85], v[96:97]
	v_pk_add_f32 v[84:85], v[82:83], v[94:95]
	v_mul_f32_e32 v82, v87, v87
	v_mul_f32_e32 v83, v89, v89
	v_fmac_f32_e32 v82, v86, v86
	v_fmac_f32_e32 v83, v88, v88
	v_add_f32_e32 v82, v82, v83
	v_mul_f32_e32 v83, v85, v85
	v_mul_f32_e32 v92, v91, v91
	v_fmac_f32_e32 v83, v84, v84
	v_fmac_f32_e32 v92, v90, v90
	v_add_f32_e32 v83, v83, v92
	v_add_f32_e32 v82, v82, v83
	v_add_f32_e32 v92, v108, v82
	v_cvt_pk_bf16_f32 v82, v86, v87
	v_cvt_pk_bf16_f32 v83, v88, v89
	v_cvt_pk_bf16_f32 v84, v84, v85
	v_cvt_pk_bf16_f32 v85, v90, v91
	v_lshl_add_u64 v[86:87], v[104:105], 0, s[0:1]
	global_store_dwordx4 v[86:87], v[82:85], off sc1
	s_nop 1
	v_mov_b32_e32 v82, v92
	s_nop 1
	v_permlane16_swap_b32_e32 v92, v82
	v_add_f32_e32 v82, v92, v82
	v_mov_b32_e32 v83, v82
	s_nop 1
	v_permlane32_swap_b32_e32 v82, v83
	s_and_saveexec_b64 s[24:25], s[4:5]
	s_cbranch_execz .LBB0_444
	v_add_f32_e32 v84, v82, v83
	v_lshlrev_b64 v[82:83], 6, v[102:103]
	v_lshl_add_u64 v[82:83], s[22:23], 0, v[82:83]
	global_store_dword v[82:83], v84, off
; __device__ __forceinline__ void st16_wt(void* p, u32x4 v) { asm volatile("global_store_dwordx4 %0, %1, off sc1\n\ts_nop 1" :: "v"(p), "v"(v) : "memory"); }
; __device__ __forceinline__ unsigned cvt_pk_bf16(float lo, float hi) { unsigned r; asm volatile("v_cvt_pk_bf16_f32 %0, %1, %2" : "=v"(r) : "v"(lo), "v"(hi)); return r; }
;     __device__ __forceinline__ void operator()(const Acc& acc, const Unit& u, int wr, int wc, int fr, int fq, const LAS float* tab) const {
;     ...
;                 const size_t row = (size_t)u.pm * BM + ai * HALF + wr * 64 + m * 16 + fr; const size_t off = row * D + col0; float ss = 0.f;
; #pragma unroll
;                 for (int bj = 0; bj < 2; ++bj) { f32x4 b0, b1;
;                     if (base32) { b0 = __builtin_nontemporal_load((const f32x4*)(base32 + off + bj * HALF)); b1 = __builtin_nontemporal_load((const f32x4*)(base32 + off + bj * HALF + 4)); }
;                     else { const u32x4 b4 = rb[ai][m][bj];
;                         b0 = (f32x4){__uint_as_float(b4.x << 16), __uint_as_float(b4.x & 0xFFFF0000u), __uint_as_float(b4.y << 16), __uint_as_float(b4.y & 0xFFFF0000u)};
;                         b1 = (f32x4){__uint_as_float(b4.z << 16), __uint_as_float(b4.z & 0xFFFF0000u), __uint_as_float(b4.w << 16), __uint_as_float(b4.w & 0xFFFF0000u)}; }
;                     const f32x4 o0 = b0 + acc[ai][bj][m][0], o1 = b1 + acc[ai][bj][m][1];
;                     if (out32) {
;                         if (!dry) { *(f32x4*)(out32 + off + bj * HALF) = o0; *(f32x4*)(out32 + off + bj * HALF + 4) = o1; }
;                         continue; }
;                     ss += ((o0[0] * o0[0] + o0[1] * o0[1]) + (o0[2] * o0[2] + o0[3] * o0[3])) + ((o1[0] * o1[0] + o1[1] * o1[1]) + (o1[2] * o1[2] + o1[3] * o1[3]));
;                     u32x4 w; w.x = cvt_pk_bf16(o0[0], o0[1]); w.y = cvt_pk_bf16(o0[2], o0[3]); w.z = cvt_pk_bf16(o1[0], o1[1]); w.w = cvt_pk_bf16(o1[2], o1[3]);
;                     if (!dry) st16_wt(xb + off + bj * HALF, w); }
;                 if (out32) continue;
;                 ss = sum_rows4(ss);
;                 if (fq == 0 && !dry) ssp[row * 16 + u.pn * 4 + wc] = ss;
.LBB0_444:
	s_or_b64 exec, exec, s[24:25]
	s_waitcnt vmcnt(9)
	v_lshlrev_b32_e32 v86, 16, v166
	v_and_b32_e32 v87, 0xffff0000, v166
	v_lshlrev_b32_e32 v88, 16, v167
	v_and_b32_e32 v89, 0xffff0000, v167
	v_lshlrev_b32_e32 v90, 16, v168
	v_and_b32_e32 v91, 0xffff0000, v168
	v_lshlrev_b32_e32 v92, 16, v169
	v_and_b32_e32 v93, 0xffff0000, v169
	v_pk_add_f32 v[80:81], v[80:81], v[88:89]
	v_pk_add_f32 v[78:79], v[78:79], v[86:87]
	v_pk_add_f32 v[86:87], v[76:77], v[92:93]
	v_pk_add_f32 v[76:77], v[74:75], v[90:91]
	v_mul_f32_e32 v74, v79, v79
	v_mul_f32_e32 v75, v81, v81
	v_fmac_f32_e32 v74, v78, v78
	v_fmac_f32_e32 v75, v80, v80
	v_add_f32_e32 v74, v74, v75
	v_mul_f32_e32 v75, v77, v77
	v_mul_f32_e32 v88, v87, v87
	v_or_b32_e32 v82, 48, v208
	v_mov_b32_e32 v83, v209
	v_fmac_f32_e32 v75, v76, v76
	v_fmac_f32_e32 v88, v86, v86
	v_lshlrev_b64 v[84:85], 11, v[82:83]
	v_add_f32_e32 v75, v75, v88
	v_lshl_add_u64 v[84:85], s[10:11], 0, v[84:85]
	v_add_f32_e32 v88, v74, v75
	v_cvt_pk_bf16_f32 v74, v78, v79
	v_cvt_pk_bf16_f32 v75, v80, v81
	v_cvt_pk_bf16_f32 v76, v76, v77
	v_cvt_pk_bf16_f32 v77, v86, v87
	v_lshl_add_u64 v[84:85], v[206:207], 1, v[84:85]
	global_store_dwordx4 v[84:85], v[74:77], off sc1
	s_nop 1
	s_waitcnt vmcnt(8)
	v_lshlrev_b32_e32 v74, 16, v162
	v_and_b32_e32 v75, 0xffff0000, v162
	v_lshlrev_b32_e32 v76, 16, v163
	v_and_b32_e32 v77, 0xffff0000, v163
	v_lshlrev_b32_e32 v78, 16, v164
	v_and_b32_e32 v79, 0xffff0000, v164
	v_lshlrev_b32_e32 v80, 16, v165
	v_and_b32_e32 v81, 0xffff0000, v165
	v_pk_add_f32 v[72:73], v[72:73], v[76:77]
	v_pk_add_f32 v[70:71], v[70:71], v[74:75]
	v_pk_add_f32 v[74:75], v[68:69], v[80:81]
	v_pk_add_f32 v[68:69], v[66:67], v[78:79]
	v_mul_f32_e32 v66, v71, v71
	v_mul_f32_e32 v67, v73, v73
	v_fmac_f32_e32 v66, v70, v70
	v_fmac_f32_e32 v67, v72, v72
	v_add_f32_e32 v66, v66, v67
	v_mul_f32_e32 v67, v69, v69
	v_mul_f32_e32 v76, v75, v75
	v_fmac_f32_e32 v67, v68, v68
	v_fmac_f32_e32 v76, v74, v74
	v_add_f32_e32 v67, v67, v76
	v_add_f32_e32 v66, v66, v67
	v_add_f32_e32 v76, v88, v66
	v_cvt_pk_bf16_f32 v66, v70, v71
	v_cvt_pk_bf16_f32 v67, v72, v73
	v_cvt_pk_bf16_f32 v68, v68, v69
	v_cvt_pk_bf16_f32 v69, v74, v75
	v_lshl_add_u64 v[70:71], v[84:85], 0, s[0:1]
	global_store_dwordx4 v[70:71], v[66:69], off sc1
	s_nop 1
	v_mov_b32_e32 v66, v76
	s_nop 1
	v_permlane16_swap_b32_e32 v76, v66
	v_add_f32_e32 v66, v76, v66
	v_mov_b32_e32 v67, v66
	s_nop 1
	v_permlane32_swap_b32_e32 v66, v67
	s_and_saveexec_b64 s[24:25], s[4:5]
	s_cbranch_execz .LBB0_446
	v_add_f32_e32 v68, v66, v67
	v_lshlrev_b64 v[66:67], 6, v[82:83]
	v_lshl_add_u64 v[66:67], s[22:23], 0, v[66:67]
	global_store_dword v[66:67], v68, off
.LBB0_446:
	s_or_b64 exec, exec, s[24:25]
	s_waitcnt vmcnt(7)
	v_lshlrev_b32_e32 v70, 16, v158
	v_and_b32_e32 v71, 0xffff0000, v158
	v_lshlrev_b32_e32 v72, 16, v159
	v_and_b32_e32 v73, 0xffff0000, v159
	v_lshlrev_b32_e32 v74, 16, v160
	v_and_b32_e32 v75, 0xffff0000, v160
	v_lshlrev_b32_e32 v76, 16, v161
	v_and_b32_e32 v77, 0xffff0000, v161
	v_pk_add_f32 v[64:65], v[64:65], v[72:73]
	v_pk_add_f32 v[62:63], v[62:63], v[70:71]
	v_pk_add_f32 v[70:71], v[60:61], v[76:77]
	v_pk_add_f32 v[60:61], v[58:59], v[74:75]
	v_mul_f32_e32 v58, v63, v63
	v_mul_f32_e32 v59, v65, v65
	v_fmac_f32_e32 v58, v62, v62
	v_fmac_f32_e32 v59, v64, v64
	v_add_f32_e32 v58, v58, v59
	v_mul_f32_e32 v59, v61, v61
	v_mul_f32_e32 v72, v71, v71
	v_lshl_add_u64 v[66:67], v[208:209], 0, s[90:91]
	v_fmac_f32_e32 v59, v60, v60
	v_fmac_f32_e32 v72, v70, v70
	v_lshlrev_b64 v[68:69], 11, v[66:67]
	v_add_f32_e32 v59, v59, v72
	v_lshl_add_u64 v[68:69], s[10:11], 0, v[68:69]
	v_add_f32_e32 v72, v58, v59
	v_cvt_pk_bf16_f32 v58, v62, v63
	v_cvt_pk_bf16_f32 v59, v64, v65
	v_cvt_pk_bf16_f32 v60, v60, v61
	v_cvt_pk_bf16_f32 v61, v70, v71
	v_lshl_add_u64 v[68:69], v[206:207], 1, v[68:69]
	global_store_dwordx4 v[68:69], v[58:61], off sc1
	s_nop 1
	s_waitcnt vmcnt(6)
	v_lshlrev_b32_e32 v58, 16, v146
	v_and_b32_e32 v59, 0xffff0000, v146
	v_lshlrev_b32_e32 v60, 16, v147
	v_and_b32_e32 v61, 0xffff0000, v147
	v_lshlrev_b32_e32 v62, 16, v148
	v_and_b32_e32 v63, 0xffff0000, v148
	v_lshlrev_b32_e32 v64, 16, v149
	v_and_b32_e32 v65, 0xffff0000, v149
	v_pk_add_f32 v[56:57], v[56:57], v[60:61]
	v_pk_add_f32 v[54:55], v[54:55], v[58:59]
	v_pk_add_f32 v[58:59], v[52:53], v[64:65]
	v_pk_add_f32 v[52:53], v[50:51], v[62:63]
	v_mul_f32_e32 v50, v55, v55
	v_mul_f32_e32 v51, v57, v57
	v_fmac_f32_e32 v50, v54, v54
	v_fmac_f32_e32 v51, v56, v56
	v_add_f32_e32 v50, v50, v51
	v_mul_f32_e32 v51, v53, v53
	v_mul_f32_e32 v60, v59, v59
	v_fmac_f32_e32 v51, v52, v52
	v_fmac_f32_e32 v60, v58, v58
	v_add_f32_e32 v51, v51, v60
	v_add_f32_e32 v50, v50, v51
	v_add_f32_e32 v60, v72, v50
	v_cvt_pk_bf16_f32 v50, v54, v55
	v_cvt_pk_bf16_f32 v51, v56, v57
	v_cvt_pk_bf16_f32 v52, v52, v53
	v_cvt_pk_bf16_f32 v53, v58, v59
	v_lshl_add_u64 v[54:55], v[68:69], 0, s[0:1]
	global_store_dwordx4 v[54:55], v[50:53], off sc1
	s_nop 1
	v_mov_b32_e32 v50, v60
	s_nop 1
	v_permlane16_swap_b32_e32 v60, v50
	v_add_f32_e32 v50, v60, v50
	v_mov_b32_e32 v51, v50
	s_nop 1
	v_permlane32_swap_b32_e32 v50, v51
	s_and_saveexec_b64 s[24:25], s[4:5]
	s_cbranch_execz .LBB0_448
	v_add_f32_e32 v52, v50, v51
	v_lshlrev_b64 v[50:51], 6, v[66:67]
	v_lshl_add_u64 v[50:51], s[22:23], 0, v[50:51]
	global_store_dword v[50:51], v52, off
; __device__ __forceinline__ void st16_wt(void* p, u32x4 v) { asm volatile("global_store_dwordx4 %0, %1, off sc1\n\ts_nop 1" :: "v"(p), "v"(v) : "memory"); }
; __device__ __forceinline__ unsigned cvt_pk_bf16(float lo, float hi) { unsigned r; asm volatile("v_cvt_pk_bf16_f32 %0, %1, %2" : "=v"(r) : "v"(lo), "v"(hi)); return r; }
;     __device__ __forceinline__ void operator()(const Acc& acc, const Unit& u, int wr, int wc, int fr, int fq, const LAS float* tab) const {
;     ...
;                 const size_t row = (size_t)u.pm * BM + ai * HALF + wr * 64 + m * 16 + fr; const size_t off = row * D + col0; float ss = 0.f;
; #pragma unroll
;                 for (int bj = 0; bj < 2; ++bj) { f32x4 b0, b1;
;                     if (base32) { b0 = __builtin_nontemporal_load((const f32x4*)(base32 + off + bj * HALF)); b1 = __builtin_nontemporal_load((const f32x4*)(base32 + off + bj * HALF + 4)); }
;                     else { const u32x4 b4 = rb[ai][m][bj];
;                         b0 = (f32x4){__uint_as_float(b4.x << 16), __uint_as_float(b4.x & 0xFFFF0000u), __uint_as_float(b4.y << 16), __uint_as_float(b4.y & 0xFFFF0000u)};
;                         b1 = (f32x4){__uint_as_float(b4.z << 16), __uint_as_float(b4.z & 0xFFFF0000u), __uint_as_float(b4.w << 16), __uint_as_float(b4.w & 0xFFFF0000u)}; }
;                     const f32x4 o0 = b0 + acc[ai][bj][m][0], o1 = b1 + acc[ai][bj][m][1];
;                     if (out32) {
;                         if (!dry) { *(f32x4*)(out32 + off + bj * HALF) = o0; *(f32x4*)(out32 + off + bj * HALF + 4) = o1; }
;                         continue; }
;                     ss += ((o0[0] * o0[0] + o0[1] * o0[1]) + (o0[2] * o0[2] + o0[3] * o0[3])) + ((o1[0] * o1[0] + o1[1] * o1[1]) + (o1[2] * o1[2] + o1[3] * o1[3]));
;                     u32x4 w; w.x = cvt_pk_bf16(o0[0], o0[1]); w.y = cvt_pk_bf16(o0[2], o0[3]); w.z = cvt_pk_bf16(o1[0], o1[1]); w.w = cvt_pk_bf16(o1[2], o1[3]);
;                     if (!dry) st16_wt(xb + off + bj * HALF, w); }
;                 if (out32) continue;
;                 ss = sum_rows4(ss);
;                 if (fq == 0 && !dry) ssp[row * 16 + u.pn * 4 + wc] = ss;
.LBB0_448:
	s_or_b64 exec, exec, s[24:25]
	s_waitcnt vmcnt(5)
	v_lshlrev_b32_e32 v54, 16, v142
	v_and_b32_e32 v55, 0xffff0000, v142
	v_lshlrev_b32_e32 v56, 16, v143
	v_and_b32_e32 v57, 0xffff0000, v143
	v_lshlrev_b32_e32 v58, 16, v144
	v_and_b32_e32 v59, 0xffff0000, v144
	v_lshlrev_b32_e32 v60, 16, v145
	v_and_b32_e32 v61, 0xffff0000, v145
	v_pk_add_f32 v[48:49], v[48:49], v[56:57]
	v_pk_add_f32 v[46:47], v[46:47], v[54:55]
	v_pk_add_f32 v[54:55], v[44:45], v[60:61]
	v_pk_add_f32 v[44:45], v[42:43], v[58:59]
	v_mul_f32_e32 v42, v47, v47
	v_mul_f32_e32 v43, v49, v49
	v_fmac_f32_e32 v42, v46, v46
	v_fmac_f32_e32 v43, v48, v48
	s_mov_b64 s[0:1], 0x90
	v_add_f32_e32 v42, v42, v43
	v_mul_f32_e32 v43, v45, v45
	v_mul_f32_e32 v56, v55, v55
	v_lshl_add_u64 v[50:51], v[208:209], 0, s[0:1]
	v_fmac_f32_e32 v43, v44, v44
	v_fmac_f32_e32 v56, v54, v54
	v_lshlrev_b64 v[52:53], 11, v[50:51]
	v_add_f32_e32 v43, v43, v56
	v_lshl_add_u64 v[52:53], s[10:11], 0, v[52:53]
	v_add_f32_e32 v56, v42, v43
	v_cvt_pk_bf16_f32 v42, v46, v47
	v_cvt_pk_bf16_f32 v43, v48, v49
	v_cvt_pk_bf16_f32 v44, v44, v45
	v_cvt_pk_bf16_f32 v45, v54, v55
	v_lshl_add_u64 v[52:53], v[206:207], 1, v[52:53]
	global_store_dwordx4 v[52:53], v[42:45], off sc1
	s_nop 1
	s_waitcnt vmcnt(4)
	v_lshlrev_b32_e32 v42, 16, v138
	v_and_b32_e32 v43, 0xffff0000, v138
	v_lshlrev_b32_e32 v44, 16, v139
	v_and_b32_e32 v45, 0xffff0000, v139
	v_lshlrev_b32_e32 v46, 16, v140
	v_and_b32_e32 v47, 0xffff0000, v140
	v_lshlrev_b32_e32 v48, 16, v141
	v_and_b32_e32 v49, 0xffff0000, v141
	v_pk_add_f32 v[40:41], v[40:41], v[44:45]
	v_pk_add_f32 v[38:39], v[38:39], v[42:43]
	v_pk_add_f32 v[42:43], v[36:37], v[48:49]
	v_pk_add_f32 v[36:37], v[34:35], v[46:47]
	v_mul_f32_e32 v34, v39, v39
	v_mul_f32_e32 v35, v41, v41
	v_fmac_f32_e32 v34, v38, v38
	v_fmac_f32_e32 v35, v40, v40
	v_add_f32_e32 v34, v34, v35
	v_mul_f32_e32 v35, v37, v37
	v_mul_f32_e32 v44, v43, v43
	v_fmac_f32_e32 v35, v36, v36
	v_fmac_f32_e32 v44, v42, v42
	v_add_f32_e32 v35, v35, v44
	v_add_f32_e32 v34, v34, v35
	v_add_f32_e32 v44, v56, v34
	v_cvt_pk_bf16_f32 v34, v38, v39
	s_mov_b64 s[0:1], 0x100
	v_cvt_pk_bf16_f32 v35, v40, v41
	v_cvt_pk_bf16_f32 v36, v36, v37
	v_cvt_pk_bf16_f32 v37, v42, v43
	v_lshl_add_u64 v[38:39], v[52:53], 0, s[0:1]
	global_store_dwordx4 v[38:39], v[34:37], off sc1
	s_nop 1
	v_mov_b32_e32 v34, v44
	s_nop 1
	v_permlane16_swap_b32_e32 v44, v34
	v_add_f32_e32 v34, v44, v34
	v_mov_b32_e32 v35, v34
	s_nop 1
	v_permlane32_swap_b32_e32 v34, v35
	s_and_saveexec_b64 s[24:25], s[4:5]
	s_cbranch_execz .LBB0_450
	v_add_f32_e32 v36, v34, v35
	v_lshlrev_b64 v[34:35], 6, v[50:51]
	v_lshl_add_u64 v[34:35], s[22:23], 0, v[34:35]
	global_store_dword v[34:35], v36, off
; __device__ __forceinline__ void st16_wt(void* p, u32x4 v) { asm volatile("global_store_dwordx4 %0, %1, off sc1\n\ts_nop 1" :: "v"(p), "v"(v) : "memory"); }
; __device__ __forceinline__ unsigned cvt_pk_bf16(float lo, float hi) { unsigned r; asm volatile("v_cvt_pk_bf16_f32 %0, %1, %2" : "=v"(r) : "v"(lo), "v"(hi)); return r; }
;     __device__ __forceinline__ void operator()(const Acc& acc, const Unit& u, int wr, int wc, int fr, int fq, const LAS float* tab) const {
;     ...
;                 const size_t row = (size_t)u.pm * BM + ai * HALF + wr * 64 + m * 16 + fr; const size_t off = row * D + col0; float ss = 0.f;
; #pragma unroll
;                 for (int bj = 0; bj < 2; ++bj) { f32x4 b0, b1;
;                     if (base32) { b0 = __builtin_nontemporal_load((const f32x4*)(base32 + off + bj * HALF)); b1 = __builtin_nontemporal_load((const f32x4*)(base32 + off + bj * HALF + 4)); }
;                     else { const u32x4 b4 = rb[ai][m][bj];
;                         b0 = (f32x4){__uint_as_float(b4.x << 16), __uint_as_float(b4.x & 0xFFFF0000u), __uint_as_float(b4.y << 16), __uint_as_float(b4.y & 0xFFFF0000u)};
;                         b1 = (f32x4){__uint_as_float(b4.z << 16), __uint_as_float(b4.z & 0xFFFF0000u), __uint_as_float(b4.w << 16), __uint_as_float(b4.w & 0xFFFF0000u)}; }
;                     const f32x4 o0 = b0 + acc[ai][bj][m][0], o1 = b1 + acc[ai][bj][m][1];
;                     if (out32) {
;                         if (!dry) { *(f32x4*)(out32 + off + bj * HALF) = o0; *(f32x4*)(out32 + off + bj * HALF + 4) = o1; }
;                         continue; }
;                     ss += ((o0[0] * o0[0] + o0[1] * o0[1]) + (o0[2] * o0[2] + o0[3] * o0[3])) + ((o1[0] * o1[0] + o1[1] * o1[1]) + (o1[2] * o1[2] + o1[3] * o1[3]));
;                     u32x4 w; w.x = cvt_pk_bf16(o0[0], o0[1]); w.y = cvt_pk_bf16(o0[2], o0[3]); w.z = cvt_pk_bf16(o1[0], o1[1]); w.w = cvt_pk_bf16(o1[2], o1[3]);
;                     if (!dry) st16_wt(xb + off + bj * HALF, w); }
;                 if (out32) continue;
;                 ss = sum_rows4(ss);
;                 if (fq == 0 && !dry) ssp[row * 16 + u.pn * 4 + wc] = ss;
.LBB0_450:
	s_or_b64 exec, exec, s[24:25]
	s_waitcnt vmcnt(3)
	v_lshlrev_b32_e32 v38, 16, v134
	v_and_b32_e32 v39, 0xffff0000, v134
	v_lshlrev_b32_e32 v40, 16, v135
	v_and_b32_e32 v41, 0xffff0000, v135
	v_lshlrev_b32_e32 v42, 16, v136
	v_and_b32_e32 v43, 0xffff0000, v136
	v_lshlrev_b32_e32 v44, 16, v137
	v_and_b32_e32 v45, 0xffff0000, v137
	v_pk_add_f32 v[32:33], v[32:33], v[40:41]
	v_pk_add_f32 v[30:31], v[30:31], v[38:39]
	v_pk_add_f32 v[38:39], v[28:29], v[44:45]
	v_pk_add_f32 v[28:29], v[26:27], v[42:43]
	v_mul_f32_e32 v26, v31, v31
	v_mul_f32_e32 v27, v33, v33
	v_fmac_f32_e32 v26, v30, v30
	v_fmac_f32_e32 v27, v32, v32
	s_mov_b64 s[0:1], 0xa0
	v_add_f32_e32 v26, v26, v27
	v_mul_f32_e32 v27, v29, v29
	v_mul_f32_e32 v40, v39, v39
	v_lshl_add_u64 v[34:35], v[208:209], 0, s[0:1]
	v_fmac_f32_e32 v27, v28, v28
	v_fmac_f32_e32 v40, v38, v38
	v_lshlrev_b64 v[36:37], 11, v[34:35]
	v_add_f32_e32 v27, v27, v40
	v_lshl_add_u64 v[36:37], s[10:11], 0, v[36:37]
	v_add_f32_e32 v40, v26, v27
	v_cvt_pk_bf16_f32 v26, v30, v31
	v_cvt_pk_bf16_f32 v27, v32, v33
	v_cvt_pk_bf16_f32 v28, v28, v29
	v_cvt_pk_bf16_f32 v29, v38, v39
	v_lshl_add_u64 v[36:37], v[206:207], 1, v[36:37]
	global_store_dwordx4 v[36:37], v[26:29], off sc1
	s_nop 1
	s_waitcnt vmcnt(2)
	v_lshlrev_b32_e32 v26, 16, v122
	v_and_b32_e32 v27, 0xffff0000, v122
	v_lshlrev_b32_e32 v28, 16, v123
	v_and_b32_e32 v29, 0xffff0000, v123
	v_lshlrev_b32_e32 v30, 16, v124
	v_and_b32_e32 v31, 0xffff0000, v124
	v_lshlrev_b32_e32 v32, 16, v125
	v_and_b32_e32 v33, 0xffff0000, v125
	v_pk_add_f32 v[24:25], v[24:25], v[28:29]
	v_pk_add_f32 v[22:23], v[22:23], v[26:27]
	v_pk_add_f32 v[26:27], v[20:21], v[32:33]
	v_pk_add_f32 v[20:21], v[18:19], v[30:31]
	v_mul_f32_e32 v18, v23, v23
	v_mul_f32_e32 v19, v25, v25
	v_fmac_f32_e32 v18, v22, v22
	v_fmac_f32_e32 v19, v24, v24
	v_add_f32_e32 v18, v18, v19
	v_mul_f32_e32 v19, v21, v21
	v_mul_f32_e32 v28, v27, v27
	v_fmac_f32_e32 v19, v20, v20
	v_fmac_f32_e32 v28, v26, v26
	v_add_f32_e32 v19, v19, v28
	v_add_f32_e32 v18, v18, v19
	v_add_f32_e32 v28, v40, v18
	v_cvt_pk_bf16_f32 v18, v22, v23
	s_mov_b64 s[0:1], 0x100
	v_cvt_pk_bf16_f32 v19, v24, v25
	v_cvt_pk_bf16_f32 v20, v20, v21
	v_cvt_pk_bf16_f32 v21, v26, v27
	v_lshl_add_u64 v[22:23], v[36:37], 0, s[0:1]
	global_store_dwordx4 v[22:23], v[18:21], off sc1
	s_nop 1
	v_mov_b32_e32 v18, v28
	s_nop 1
	v_permlane16_swap_b32_e32 v28, v18
	v_add_f32_e32 v18, v28, v18
	v_mov_b32_e32 v19, v18
	s_nop 1
	v_permlane32_swap_b32_e32 v18, v19
	s_and_saveexec_b64 s[24:25], s[4:5]
	s_cbranch_execz .LBB0_452
	v_add_f32_e32 v20, v18, v19
	v_lshlrev_b64 v[18:19], 6, v[34:35]
	v_lshl_add_u64 v[18:19], s[22:23], 0, v[18:19]
	global_store_dword v[18:19], v20, off
.LBB0_452:
	s_or_b64 exec, exec, s[24:25]
	s_waitcnt vmcnt(1)
	v_lshlrev_b32_e32 v22, 16, v110
	v_and_b32_e32 v23, 0xffff0000, v110
	v_lshlrev_b32_e32 v24, 16, v111
	v_and_b32_e32 v25, 0xffff0000, v111
	v_lshlrev_b32_e32 v26, 16, v112
	v_and_b32_e32 v27, 0xffff0000, v112
	v_lshlrev_b32_e32 v28, 16, v113
	v_and_b32_e32 v29, 0xffff0000, v113
	v_pk_add_f32 v[16:17], v[16:17], v[24:25]
	v_pk_add_f32 v[14:15], v[14:15], v[22:23]
	v_pk_add_f32 v[22:23], v[12:13], v[28:29]
	v_pk_add_f32 v[12:13], v[10:11], v[26:27]
	v_mul_f32_e32 v10, v15, v15
	v_mul_f32_e32 v11, v17, v17
	v_fmac_f32_e32 v10, v14, v14
	v_fmac_f32_e32 v11, v16, v16
	s_mov_b64 s[0:1], 0xb0
	v_add_f32_e32 v10, v10, v11
	v_mul_f32_e32 v11, v13, v13
	v_mul_f32_e32 v24, v23, v23
	v_lshl_add_u64 v[18:19], v[208:209], 0, s[0:1]
	v_fmac_f32_e32 v11, v12, v12
	v_fmac_f32_e32 v24, v22, v22
	v_lshlrev_b64 v[20:21], 11, v[18:19]
	v_add_f32_e32 v11, v11, v24
	v_lshl_add_u64 v[20:21], s[10:11], 0, v[20:21]
	v_add_f32_e32 v24, v10, v11
	v_cvt_pk_bf16_f32 v10, v14, v15
	v_cvt_pk_bf16_f32 v11, v16, v17
	v_cvt_pk_bf16_f32 v12, v12, v13
	v_cvt_pk_bf16_f32 v13, v22, v23
	v_lshl_add_u64 v[20:21], v[206:207], 1, v[20:21]
	global_store_dwordx4 v[20:21], v[10:13], off sc1
	s_nop 1
	s_waitcnt vmcnt(0)
	v_lshlrev_b32_e32 v10, 16, v98
	v_and_b32_e32 v11, 0xffff0000, v98
	v_lshlrev_b32_e32 v12, 16, v99
	v_and_b32_e32 v13, 0xffff0000, v99
	v_lshlrev_b32_e32 v14, 16, v100
	v_and_b32_e32 v15, 0xffff0000, v100
	v_lshlrev_b32_e32 v16, 16, v101
	v_and_b32_e32 v17, 0xffff0000, v101
	v_pk_add_f32 v[8:9], v[8:9], v[12:13]
	v_pk_add_f32 v[6:7], v[6:7], v[10:11]
	v_pk_add_f32 v[10:11], v[4:5], v[16:17]
	v_pk_add_f32 v[4:5], v[2:3], v[14:15]
	v_mul_f32_e32 v2, v7, v7
	v_mul_f32_e32 v3, v9, v9
	v_fmac_f32_e32 v2, v6, v6
	v_fmac_f32_e32 v3, v8, v8
	v_add_f32_e32 v2, v2, v3
	v_mul_f32_e32 v3, v5, v5
	v_mul_f32_e32 v12, v11, v11
	v_fmac_f32_e32 v3, v4, v4
	v_fmac_f32_e32 v12, v10, v10
	v_add_f32_e32 v3, v3, v12
	v_add_f32_e32 v2, v2, v3
	v_add_f32_e32 v12, v24, v2
	v_cvt_pk_bf16_f32 v2, v6, v7
	s_mov_b64 s[0:1], 0x100
	v_cvt_pk_bf16_f32 v3, v8, v9
	v_cvt_pk_bf16_f32 v4, v4, v5
	v_cvt_pk_bf16_f32 v5, v10, v11
	v_lshl_add_u64 v[6:7], v[20:21], 0, s[0:1]
	global_store_dwordx4 v[6:7], v[2:5], off sc1
	s_nop 1
	v_mov_b32_e32 v2, v12
	s_nop 1
	v_permlane16_swap_b32_e32 v12, v2
	v_add_f32_e32 v2, v12, v2
	v_mov_b32_e32 v3, v2
	s_nop 1
	v_permlane32_swap_b32_e32 v2, v3
	s_and_saveexec_b64 s[24:25], s[4:5]
	s_cbranch_execz .LBB0_454
	v_add_f32_e32 v4, v2, v3
	v_lshlrev_b64 v[2:3], 6, v[18:19]
	v_lshl_add_u64 v[2:3], s[22:23], 0, v[2:3]
	global_store_dword v[2:3], v4, off

;     __device__ __forceinline__ void operator()(const Acc& acc, const Unit& u, int wr, int wc, int fr, int fq, const LAS float* tab) const {
;     ...
;                     for (int bj = 0; bj < 2; ++bj) rb[ai][m][bj] = *(const u32x4*)(xb + ((size_t)u.pm * BM + ai * HALF + wr * 64 + m * 16 + fr) * D + col0 + bj * HALF);
;     ...
;                 for (int bj = 0; bj < 2; ++bj) { f32x4 b0, b1;
;                     if (base32) { b0 = __builtin_nontemporal_load((const f32x4*)(base32 + off + bj * HALF)); b1 = __builtin_nontemporal_load((const f32x4*)(base32 + off + bj * HALF + 4)); }
;                     else { const u32x4 b4 = rb[ai][m][bj];
;                         b0 = (f32x4){__uint_as_float(b4.x << 16), __uint_as_float(b4.x & 0xFFFF0000u), __uint_as_float(b4.y << 16), __uint_as_float(b4.y & 0xFFFF0000u)};
;                         b1 = (f32x4){__uint_as_float(b4.z << 16), __uint_as_float(b4.z & 0xFFFF0000u), __uint_as_float(b4.w << 16), __uint_as_float(b4.w & 0xFFFF0000u)}; }
.LBB0_1862:
	s_ashr_i32 s9, s8, 31
	v_lshl_or_b32 v218, s30, 8, v237
	s_lshl_b64 s[0:1], s[8:9], 8
	v_lshl_add_u64 v[220:221], s[0:1], 0, v[212:213]
	s_andn2_b64 vcc, exec, s[16:17]
	v_ashrrev_i32_e32 v219, 31, v218
	s_cbranch_vccnz .LBB0_1864
	v_lshl_add_u64 v[66:67], v[218:219], 1, s[14:15]
	v_lshlrev_b64 v[68:69], 11, v[220:221]
	v_lshl_add_u64 v[66:67], v[66:67], 0, v[68:69]
	v_add_co_u32_e32 v68, vcc, 0x8000, v66
	global_load_dwordx4 v[190:193], v[66:67], off
	global_load_dwordx4 v[186:189], v[66:67], off offset:256
	v_addc_co_u32_e32 v69, vcc, 0, v67, vcc
	global_load_dwordx4 v[182:185], v[68:69], off
	global_load_dwordx4 v[178:181], v[68:69], off offset:256
	v_add_co_u32_e32 v68, vcc, 0x10000, v66
	s_nop 1
	v_addc_co_u32_e32 v69, vcc, 0, v67, vcc
	global_load_dwordx4 v[174:177], v[68:69], off
	global_load_dwordx4 v[170:173], v[68:69], off offset:256
	v_add_co_u32_e32 v68, vcc, 0x18000, v66
	s_nop 1
	v_addc_co_u32_e32 v69, vcc, 0, v67, vcc
	global_load_dwordx4 v[166:169], v[68:69], off
	global_load_dwordx4 v[154:157], v[68:69], off offset:256
	v_add_co_u32_e32 v68, vcc, 0x40000, v66
	s_nop 1
	v_addc_co_u32_e32 v69, vcc, 0, v67, vcc
	global_load_dwordx4 v[142:145], v[68:69], off
	global_load_dwordx4 v[138:141], v[68:69], off offset:256
	v_add_co_u32_e32 v68, vcc, 0x48000, v66
	s_nop 1
	v_addc_co_u32_e32 v69, vcc, 0, v67, vcc
	global_load_dwordx4 v[122:125], v[68:69], off
	global_load_dwordx4 v[114:117], v[68:69], off offset:256
	v_add_co_u32_e32 v68, vcc, 0x50000, v66
	s_nop 1
	v_addc_co_u32_e32 v69, vcc, 0, v67, vcc
	v_add_co_u32_e32 v66, vcc, 0x58000, v66
	global_load_dwordx4 v[102:105], v[68:69], off
	global_load_dwordx4 v[90:93], v[68:69], off offset:256
	v_addc_co_u32_e32 v67, vcc, 0, v67, vcc
	global_load_dwordx4 v[78:81], v[66:67], off
	s_nop 0
	global_load_dwordx4 v[66:69], v[66:67], off offset:256
.LBB0_1864:
	v_lshlrev_b64 v[194:195], 10, v[220:221]
	v_lshl_add_u64 v[224:225], v[194:195], 0, v[218:219]
	v_cndmask_b32_e64 v194, 0, 1, s[18:19]
	s_mov_b64 s[34:35], -1
	v_cmp_ne_u32_e64 s[8:9], 1, v194
	s_andn2_b64 vcc, exec, s[18:19]
	v_lshl_add_u64 v[222:223], v[224:225], 2, s[10:11]
	s_cbranch_vccnz .LBB0_1866
	global_load_dwordx4 v[198:201], v[222:223], off offset:16 nt
	global_load_dwordx4 v[194:197], v[222:223], off nt
	global_load_dwordx4 v[244:247], v[222:223], off offset:528 nt
	global_load_dwordx4 v[248:251], v[222:223], off offset:512 nt
	s_waitcnt vmcnt(0)
	s_mov_b64 s[34:35], 0
.LBB0_1866:
	s_andn2_b64 vcc, exec, s[34:35]
	s_cbranch_vccnz .LBB0_1868
	s_waitcnt vmcnt(15)
	v_lshlrev_b32_e32 v194, 16, v190
	v_and_b32_e32 v195, 0xffff0000, v190
	v_lshlrev_b32_e32 v196, 16, v191
	v_and_b32_e32 v197, 0xffff0000, v191
	v_lshlrev_b32_e32 v198, 16, v192
	v_and_b32_e32 v199, 0xffff0000, v192
	v_lshlrev_b32_e32 v200, 16, v193
	v_and_b32_e32 v201, 0xffff0000, v193

;     __device__ __forceinline__ void operator()(const Acc& acc, const Unit& u, int wr, int wc, int fr, int fq, const LAS float* tab) const {
;     ...
;                     else { const u32x4 b4 = rb[ai][m][bj];
;                         b0 = (f32x4){__uint_as_float(b4.x << 16), __uint_as_float(b4.x & 0xFFFF0000u), __uint_as_float(b4.y << 16), __uint_as_float(b4.y & 0xFFFF0000u)};
;                         b1 = (f32x4){__uint_as_float(b4.z << 16), __uint_as_float(b4.z & 0xFFFF0000u), __uint_as_float(b4.w << 16), __uint_as_float(b4.w & 0xFFFF0000u)}; }
.LBB0_1870:
	s_andn2_b64 vcc, exec, s[34:35]
	s_cbranch_vccnz .LBB0_1872
	s_waitcnt vmcnt(14)
	v_lshlrev_b32_e32 v158, 16, v186
	v_and_b32_e32 v159, 0xffff0000, v186
	v_lshlrev_b32_e32 v160, 16, v187
	v_and_b32_e32 v161, 0xffff0000, v187
	v_lshlrev_b32_e32 v162, 16, v188
	v_and_b32_e32 v163, 0xffff0000, v188
	v_lshlrev_b32_e32 v164, 16, v189
	v_and_b32_e32 v165, 0xffff0000, v189

;     __device__ __forceinline__ void operator()(const Acc& acc, const Unit& u, int wr, int wc, int fr, int fq, const LAS float* tab) const {
;     ...
;                     else { const u32x4 b4 = rb[ai][m][bj];
;                         b0 = (f32x4){__uint_as_float(b4.x << 16), __uint_as_float(b4.x & 0xFFFF0000u), __uint_as_float(b4.y << 16), __uint_as_float(b4.y & 0xFFFF0000u)};
;                         b1 = (f32x4){__uint_as_float(b4.z << 16), __uint_as_float(b4.z & 0xFFFF0000u), __uint_as_float(b4.w << 16), __uint_as_float(b4.w & 0xFFFF0000u)}; }
.LBB0_1876:
	s_andn2_b64 vcc, exec, s[34:35]
	s_cbranch_vccnz .LBB0_1878
	s_waitcnt vmcnt(13)
	v_lshlrev_b32_e32 v146, 16, v182
	v_and_b32_e32 v147, 0xffff0000, v182
	v_lshlrev_b32_e32 v148, 16, v183
	v_and_b32_e32 v149, 0xffff0000, v183
	v_lshlrev_b32_e32 v150, 16, v184
	v_and_b32_e32 v151, 0xffff0000, v184
	v_lshlrev_b32_e32 v152, 16, v185
	v_and_b32_e32 v153, 0xffff0000, v185

;     __device__ __forceinline__ void operator()(const Acc& acc, const Unit& u, int wr, int wc, int fr, int fq, const LAS float* tab) const {
;     ...
;                     else { const u32x4 b4 = rb[ai][m][bj];
;                         b0 = (f32x4){__uint_as_float(b4.x << 16), __uint_as_float(b4.x & 0xFFFF0000u), __uint_as_float(b4.y << 16), __uint_as_float(b4.y & 0xFFFF0000u)};
;                         b1 = (f32x4){__uint_as_float(b4.z << 16), __uint_as_float(b4.z & 0xFFFF0000u), __uint_as_float(b4.w << 16), __uint_as_float(b4.w & 0xFFFF0000u)}; }
.LBB0_1880:
	s_andn2_b64 vcc, exec, s[34:35]
	s_cbranch_vccnz .LBB0_1882
	s_waitcnt vmcnt(12)
	v_lshlrev_b32_e32 v130, 16, v178
	v_and_b32_e32 v131, 0xffff0000, v178
	v_lshlrev_b32_e32 v132, 16, v179
	v_and_b32_e32 v133, 0xffff0000, v179
	v_lshlrev_b32_e32 v134, 16, v180
	v_and_b32_e32 v135, 0xffff0000, v180
	v_lshlrev_b32_e32 v136, 16, v181
	v_and_b32_e32 v137, 0xffff0000, v181

;     __device__ __forceinline__ void operator()(const Acc& acc, const Unit& u, int wr, int wc, int fr, int fq, const LAS float* tab) const {
;     ...
;                     else { const u32x4 b4 = rb[ai][m][bj];
;                         b0 = (f32x4){__uint_as_float(b4.x << 16), __uint_as_float(b4.x & 0xFFFF0000u), __uint_as_float(b4.y << 16), __uint_as_float(b4.y & 0xFFFF0000u)};
;                         b1 = (f32x4){__uint_as_float(b4.z << 16), __uint_as_float(b4.z & 0xFFFF0000u), __uint_as_float(b4.w << 16), __uint_as_float(b4.w & 0xFFFF0000u)}; }
.LBB0_1886:
	s_andn2_b64 vcc, exec, s[34:35]
	s_cbranch_vccnz .LBB0_1888
	s_waitcnt vmcnt(11)
	v_lshlrev_b32_e32 v118, 16, v174
	v_and_b32_e32 v119, 0xffff0000, v174
	v_lshlrev_b32_e32 v120, 16, v175
	v_and_b32_e32 v121, 0xffff0000, v175
	v_lshlrev_b32_e32 v126, 16, v176
	v_and_b32_e32 v127, 0xffff0000, v176
	v_lshlrev_b32_e32 v128, 16, v177
	v_and_b32_e32 v129, 0xffff0000, v177

;     __device__ __forceinline__ void operator()(const Acc& acc, const Unit& u, int wr, int wc, int fr, int fq, const LAS float* tab) const {
;     ...
;                     else { const u32x4 b4 = rb[ai][m][bj];
;                         b0 = (f32x4){__uint_as_float(b4.x << 16), __uint_as_float(b4.x & 0xFFFF0000u), __uint_as_float(b4.y << 16), __uint_as_float(b4.y & 0xFFFF0000u)};
;                         b1 = (f32x4){__uint_as_float(b4.z << 16), __uint_as_float(b4.z & 0xFFFF0000u), __uint_as_float(b4.w << 16), __uint_as_float(b4.w & 0xFFFF0000u)}; }
.LBB0_1890:
	s_andn2_b64 vcc, exec, s[34:35]
	s_cbranch_vccnz .LBB0_1892
	s_waitcnt vmcnt(10)
	v_lshlrev_b32_e32 v106, 16, v170
	v_and_b32_e32 v107, 0xffff0000, v170
	v_lshlrev_b32_e32 v108, 16, v171
	v_and_b32_e32 v109, 0xffff0000, v171
	v_lshlrev_b32_e32 v110, 16, v172
	v_and_b32_e32 v111, 0xffff0000, v172
	v_lshlrev_b32_e32 v112, 16, v173
	v_and_b32_e32 v113, 0xffff0000, v173

;     __device__ __forceinline__ void operator()(const Acc& acc, const Unit& u, int wr, int wc, int fr, int fq, const LAS float* tab) const {
;     ...
;                     else { const u32x4 b4 = rb[ai][m][bj];
;                         b0 = (f32x4){__uint_as_float(b4.x << 16), __uint_as_float(b4.x & 0xFFFF0000u), __uint_as_float(b4.y << 16), __uint_as_float(b4.y & 0xFFFF0000u)};
;                         b1 = (f32x4){__uint_as_float(b4.z << 16), __uint_as_float(b4.z & 0xFFFF0000u), __uint_as_float(b4.w << 16), __uint_as_float(b4.w & 0xFFFF0000u)}; }
.LBB0_1896:
	s_andn2_b64 vcc, exec, s[34:35]
	s_cbranch_vccnz .LBB0_1898
	s_waitcnt vmcnt(9)
	v_lshlrev_b32_e32 v94, 16, v166
	v_and_b32_e32 v95, 0xffff0000, v166
	v_lshlrev_b32_e32 v96, 16, v167
	v_and_b32_e32 v97, 0xffff0000, v167
	v_lshlrev_b32_e32 v98, 16, v168
	v_and_b32_e32 v99, 0xffff0000, v168
	v_lshlrev_b32_e32 v100, 16, v169
	v_and_b32_e32 v101, 0xffff0000, v169

;     __device__ __forceinline__ void operator()(const Acc& acc, const Unit& u, int wr, int wc, int fr, int fq, const LAS float* tab) const {
;     ...
;                     else { const u32x4 b4 = rb[ai][m][bj];
;                         b0 = (f32x4){__uint_as_float(b4.x << 16), __uint_as_float(b4.x & 0xFFFF0000u), __uint_as_float(b4.y << 16), __uint_as_float(b4.y & 0xFFFF0000u)};
;                         b1 = (f32x4){__uint_as_float(b4.z << 16), __uint_as_float(b4.z & 0xFFFF0000u), __uint_as_float(b4.w << 16), __uint_as_float(b4.w & 0xFFFF0000u)}; }
.LBB0_1900:
	s_andn2_b64 vcc, exec, s[34:35]
	s_cbranch_vccnz .LBB0_1902
	s_waitcnt vmcnt(8)
	v_lshlrev_b32_e32 v82, 16, v154
	v_and_b32_e32 v83, 0xffff0000, v154
	v_lshlrev_b32_e32 v84, 16, v155
	v_and_b32_e32 v85, 0xffff0000, v155
	v_lshlrev_b32_e32 v86, 16, v156
	v_and_b32_e32 v87, 0xffff0000, v156
	v_lshlrev_b32_e32 v88, 16, v157
	v_and_b32_e32 v89, 0xffff0000, v157

;     __device__ __forceinline__ void operator()(const Acc& acc, const Unit& u, int wr, int wc, int fr, int fq, const LAS float* tab) const {
;     ...
;                     else { const u32x4 b4 = rb[ai][m][bj];
;                         b0 = (f32x4){__uint_as_float(b4.x << 16), __uint_as_float(b4.x & 0xFFFF0000u), __uint_as_float(b4.y << 16), __uint_as_float(b4.y & 0xFFFF0000u)};
;                         b1 = (f32x4){__uint_as_float(b4.z << 16), __uint_as_float(b4.z & 0xFFFF0000u), __uint_as_float(b4.w << 16), __uint_as_float(b4.w & 0xFFFF0000u)}; }
.LBB0_1906:
	s_andn2_b64 vcc, exec, s[34:35]
	s_cbranch_vccnz .LBB0_1908
	s_waitcnt vmcnt(7)
	v_lshlrev_b32_e32 v70, 16, v142
	v_and_b32_e32 v71, 0xffff0000, v142
	v_lshlrev_b32_e32 v72, 16, v143
	v_and_b32_e32 v73, 0xffff0000, v143
	v_lshlrev_b32_e32 v74, 16, v144
	v_and_b32_e32 v75, 0xffff0000, v144
	v_lshlrev_b32_e32 v76, 16, v145
	v_and_b32_e32 v77, 0xffff0000, v145

;     __device__ __forceinline__ void operator()(const Acc& acc, const Unit& u, int wr, int wc, int fr, int fq, const LAS float* tab) const {
;     ...
;                     else { const u32x4 b4 = rb[ai][m][bj];
;                         b0 = (f32x4){__uint_as_float(b4.x << 16), __uint_as_float(b4.x & 0xFFFF0000u), __uint_as_float(b4.y << 16), __uint_as_float(b4.y & 0xFFFF0000u)};
;                         b1 = (f32x4){__uint_as_float(b4.z << 16), __uint_as_float(b4.z & 0xFFFF0000u), __uint_as_float(b4.w << 16), __uint_as_float(b4.w & 0xFFFF0000u)}; }
.LBB0_1910:
	s_andn2_b64 vcc, exec, s[34:35]
	s_cbranch_vccnz .LBB0_1912
	s_waitcnt vmcnt(6)
	v_lshlrev_b32_e32 v58, 16, v138
	v_and_b32_e32 v59, 0xffff0000, v138
	v_lshlrev_b32_e32 v60, 16, v139
	v_and_b32_e32 v61, 0xffff0000, v139
	v_lshlrev_b32_e32 v62, 16, v140
	v_and_b32_e32 v63, 0xffff0000, v140
	v_lshlrev_b32_e32 v64, 16, v141
	v_and_b32_e32 v65, 0xffff0000, v141

;     __device__ __forceinline__ void operator()(const Acc& acc, const Unit& u, int wr, int wc, int fr, int fq, const LAS float* tab) const {
;     ...
;                     else { const u32x4 b4 = rb[ai][m][bj];
;                         b0 = (f32x4){__uint_as_float(b4.x << 16), __uint_as_float(b4.x & 0xFFFF0000u), __uint_as_float(b4.y << 16), __uint_as_float(b4.y & 0xFFFF0000u)};
;                         b1 = (f32x4){__uint_as_float(b4.z << 16), __uint_as_float(b4.z & 0xFFFF0000u), __uint_as_float(b4.w << 16), __uint_as_float(b4.w & 0xFFFF0000u)}; }
.LBB0_1916:
	s_andn2_b64 vcc, exec, s[34:35]
	s_cbranch_vccnz .LBB0_1918
	s_waitcnt vmcnt(5)
	v_lshlrev_b32_e32 v50, 16, v122
	v_and_b32_e32 v51, 0xffff0000, v122
	v_lshlrev_b32_e32 v52, 16, v123
	v_and_b32_e32 v53, 0xffff0000, v123
	v_lshlrev_b32_e32 v54, 16, v124
	v_and_b32_e32 v55, 0xffff0000, v124
	v_lshlrev_b32_e32 v56, 16, v125
	v_and_b32_e32 v57, 0xffff0000, v125

;     __device__ __forceinline__ void operator()(const Acc& acc, const Unit& u, int wr, int wc, int fr, int fq, const LAS float* tab) const {
;     ...
;                     else { const u32x4 b4 = rb[ai][m][bj];
;                         b0 = (f32x4){__uint_as_float(b4.x << 16), __uint_as_float(b4.x & 0xFFFF0000u), __uint_as_float(b4.y << 16), __uint_as_float(b4.y & 0xFFFF0000u)};
;                         b1 = (f32x4){__uint_as_float(b4.z << 16), __uint_as_float(b4.z & 0xFFFF0000u), __uint_as_float(b4.w << 16), __uint_as_float(b4.w & 0xFFFF0000u)}; }
.LBB0_1920:
	s_andn2_b64 vcc, exec, s[34:35]
	s_cbranch_vccnz .LBB0_1922
	s_waitcnt vmcnt(4)
	v_lshlrev_b32_e32 v42, 16, v114
	v_and_b32_e32 v43, 0xffff0000, v114
	v_lshlrev_b32_e32 v44, 16, v115
	v_and_b32_e32 v45, 0xffff0000, v115
	v_lshlrev_b32_e32 v46, 16, v116
	v_and_b32_e32 v47, 0xffff0000, v116
	v_lshlrev_b32_e32 v48, 16, v117
	v_and_b32_e32 v49, 0xffff0000, v117

;     __device__ __forceinline__ void operator()(const Acc& acc, const Unit& u, int wr, int wc, int fr, int fq, const LAS float* tab) const {
;     ...
;                     else { const u32x4 b4 = rb[ai][m][bj];
;                         b0 = (f32x4){__uint_as_float(b4.x << 16), __uint_as_float(b4.x & 0xFFFF0000u), __uint_as_float(b4.y << 16), __uint_as_float(b4.y & 0xFFFF0000u)};
;                         b1 = (f32x4){__uint_as_float(b4.z << 16), __uint_as_float(b4.z & 0xFFFF0000u), __uint_as_float(b4.w << 16), __uint_as_float(b4.w & 0xFFFF0000u)}; }
.LBB0_1926:
	s_andn2_b64 vcc, exec, s[34:35]
	s_cbranch_vccnz .LBB0_1928
	s_waitcnt vmcnt(3)
	v_lshlrev_b32_e32 v34, 16, v102
	v_and_b32_e32 v35, 0xffff0000, v102
	v_lshlrev_b32_e32 v36, 16, v103
	v_and_b32_e32 v37, 0xffff0000, v103
	v_lshlrev_b32_e32 v38, 16, v104
	v_and_b32_e32 v39, 0xffff0000, v104
	v_lshlrev_b32_e32 v40, 16, v105
	v_and_b32_e32 v41, 0xffff0000, v105

;     __device__ __forceinline__ void operator()(const Acc& acc, const Unit& u, int wr, int wc, int fr, int fq, const LAS float* tab) const {
;     ...
;                     else { const u32x4 b4 = rb[ai][m][bj];
;                         b0 = (f32x4){__uint_as_float(b4.x << 16), __uint_as_float(b4.x & 0xFFFF0000u), __uint_as_float(b4.y << 16), __uint_as_float(b4.y & 0xFFFF0000u)};
;                         b1 = (f32x4){__uint_as_float(b4.z << 16), __uint_as_float(b4.z & 0xFFFF0000u), __uint_as_float(b4.w << 16), __uint_as_float(b4.w & 0xFFFF0000u)}; }
.LBB0_1930:
	s_andn2_b64 vcc, exec, s[34:35]
	s_cbranch_vccnz .LBB0_1932
	s_waitcnt vmcnt(2)
	v_lshlrev_b32_e32 v26, 16, v90
	v_and_b32_e32 v27, 0xffff0000, v90
	v_lshlrev_b32_e32 v28, 16, v91
	v_and_b32_e32 v29, 0xffff0000, v91
	v_lshlrev_b32_e32 v30, 16, v92
	v_and_b32_e32 v31, 0xffff0000, v92
	v_lshlrev_b32_e32 v32, 16, v93
	v_and_b32_e32 v33, 0xffff0000, v93

;     __device__ __forceinline__ void operator()(const Acc& acc, const Unit& u, int wr, int wc, int fr, int fq, const LAS float* tab) const {
;     ...
;                     else { const u32x4 b4 = rb[ai][m][bj];
;                         b0 = (f32x4){__uint_as_float(b4.x << 16), __uint_as_float(b4.x & 0xFFFF0000u), __uint_as_float(b4.y << 16), __uint_as_float(b4.y & 0xFFFF0000u)};
;                         b1 = (f32x4){__uint_as_float(b4.z << 16), __uint_as_float(b4.z & 0xFFFF0000u), __uint_as_float(b4.w << 16), __uint_as_float(b4.w & 0xFFFF0000u)}; }
.LBB0_1936:
	s_andn2_b64 vcc, exec, s[34:35]
	s_cbranch_vccnz .LBB0_1938
	s_waitcnt vmcnt(1)
	v_lshlrev_b32_e32 v18, 16, v78
	v_and_b32_e32 v19, 0xffff0000, v78
	v_lshlrev_b32_e32 v20, 16, v79
	v_and_b32_e32 v21, 0xffff0000, v79
	v_lshlrev_b32_e32 v22, 16, v80
	v_and_b32_e32 v23, 0xffff0000, v80
	v_lshlrev_b32_e32 v24, 16, v81
	v_and_b32_e32 v25, 0xffff0000, v81

;     __device__ __forceinline__ void operator()(const Acc& acc, const Unit& u, int wr, int wc, int fr, int fq, const LAS float* tab) const {
;     ...
;                     for (int bj = 0; bj < 2; ++bj) rb[ai][m][bj] = *(const u32x4*)(xb + ((size_t)u.pm * BM + ai * HALF + wr * 64 + m * 16 + fr) * D + col0 + bj * HALF);
;     ...
;                 for (int bj = 0; bj < 2; ++bj) { f32x4 b0, b1;
;                     if (base32) { b0 = __builtin_nontemporal_load((const f32x4*)(base32 + off + bj * HALF)); b1 = __builtin_nontemporal_load((const f32x4*)(base32 + off + bj * HALF + 4)); }
;                     else { const u32x4 b4 = rb[ai][m][bj];
;                         b0 = (f32x4){__uint_as_float(b4.x << 16), __uint_as_float(b4.x & 0xFFFF0000u), __uint_as_float(b4.y << 16), __uint_as_float(b4.y & 0xFFFF0000u)};
;                         b1 = (f32x4){__uint_as_float(b4.z << 16), __uint_as_float(b4.z & 0xFFFF0000u), __uint_as_float(b4.w << 16), __uint_as_float(b4.w & 0xFFFF0000u)}; }
;                     const f32x4 o0 = b0 + acc[ai][bj][m][0], o1 = b1 + acc[ai][bj][m][1];
;                     if (out32) {
;                         if (!dry) { *(f32x4*)(out32 + off + bj * HALF) = o0; *(f32x4*)(out32 + off + bj * HALF + 4) = o1; }
;                         continue; }
.LBB0_2181:
	s_ashr_i32 s13, s12, 31
	v_lshl_or_b32 v208, s2, 8, v217
	s_lshl_b64 s[0:1], s[12:13], 8
	v_lshl_add_u64 v[210:211], s[0:1], 0, v[196:197]
	v_ashrrev_i32_e32 v209, 31, v208
	v_lshl_add_u64 v[206:207], v[208:209], 1, s[20:21]
	v_lshlrev_b64 v[66:67], 11, v[210:211]
	v_lshl_add_u64 v[212:213], v[206:207], 0, v[66:67]
	v_add_co_u32_e32 v66, vcc, 0x8000, v212
	global_load_dwordx4 v[220:223], v[212:213], off
	global_load_dwordx4 v[186:189], v[212:213], off offset:256
	v_addc_co_u32_e32 v67, vcc, 0, v213, vcc
	global_load_dwordx4 v[182:185], v[66:67], off
	global_load_dwordx4 v[178:181], v[66:67], off offset:256
	v_add_co_u32_e32 v66, vcc, 0x10000, v212
	v_cndmask_b32_e64 v214, 0, 1, s[24:25]
	s_nop 0
	v_addc_co_u32_e32 v67, vcc, 0, v213, vcc
	global_load_dwordx4 v[174:177], v[66:67], off
	global_load_dwordx4 v[170:173], v[66:67], off offset:256
	v_add_co_u32_e32 v66, vcc, 0x18000, v212
	v_cmp_ne_u32_e64 s[10:11], 1, v214
	s_nop 0
	v_addc_co_u32_e32 v67, vcc, 0, v213, vcc
	global_load_dwordx4 v[166:169], v[66:67], off
	global_load_dwordx4 v[154:157], v[66:67], off offset:256
	v_add_co_u32_e32 v66, vcc, 0x40000, v212
	v_lshlrev_b64 v[214:215], 10, v[210:211]
	s_nop 0
	v_addc_co_u32_e32 v67, vcc, 0, v213, vcc
	global_load_dwordx4 v[146:149], v[66:67], off
	global_load_dwordx4 v[138:141], v[66:67], off offset:256
	v_add_co_u32_e32 v66, vcc, 0x48000, v212
	v_lshl_add_u64 v[214:215], v[214:215], 0, v[208:209]
	s_nop 0
	v_addc_co_u32_e32 v67, vcc, 0, v213, vcc
	global_load_dwordx4 v[126:129], v[66:67], off
	global_load_dwordx4 v[114:117], v[66:67], off offset:256
	v_add_co_u32_e32 v66, vcc, 0x50000, v212
	s_mov_b64 s[12:13], -1
	s_nop 0
	v_addc_co_u32_e32 v67, vcc, 0, v213, vcc
	global_load_dwordx4 v[102:105], v[66:67], off
	global_load_dwordx4 v[90:93], v[66:67], off offset:256
	v_add_co_u32_e32 v66, vcc, 0x58000, v212
	v_lshl_add_u64 v[214:215], v[214:215], 2, s[18:19]
	s_nop 0
	v_addc_co_u32_e32 v67, vcc, 0, v213, vcc
	global_load_dwordx4 v[78:81], v[66:67], off
	s_nop 0
	global_load_dwordx4 v[66:69], v[66:67], off offset:256
	s_andn2_b64 vcc, exec, s[24:25]
	s_nop 0
	s_waitcnt vmcnt(15)
	v_lshlrev_b32_e32 v224, 16, v220
	v_and_b32_e32 v225, 0xffff0000, v220
	v_lshlrev_b32_e32 v220, 16, v221
	v_and_b32_e32 v221, 0xffff0000, v221
	v_lshlrev_b32_e32 v226, 16, v222
	v_and_b32_e32 v227, 0xffff0000, v222
	v_lshlrev_b32_e32 v222, 16, v223
	v_and_b32_e32 v223, 0xffff0000, v223
	v_pk_add_f32 v[164:165], v[164:165], v[220:221]
	v_pk_add_f32 v[162:163], v[162:163], v[224:225]
	v_pk_add_f32 v[160:161], v[160:161], v[222:223]
	v_pk_add_f32 v[158:159], v[158:159], v[226:227]
	s_cbranch_vccnz .LBB0_2183
	s_mov_b64 s[12:13], 0
	global_store_dwordx4 v[214:215], v[162:165], off
	global_store_dwordx4 v[214:215], v[158:161], off offset:16

;     __device__ __forceinline__ void operator()(const Acc& acc, const Unit& u, int wr, int wc, int fr, int fq, const LAS float* tab) const {
;     ...
;                     else { const u32x4 b4 = rb[ai][m][bj];
;                         b0 = (f32x4){__uint_as_float(b4.x << 16), __uint_as_float(b4.x & 0xFFFF0000u), __uint_as_float(b4.y << 16), __uint_as_float(b4.y & 0xFFFF0000u)};
;                         b1 = (f32x4){__uint_as_float(b4.z << 16), __uint_as_float(b4.z & 0xFFFF0000u), __uint_as_float(b4.w << 16), __uint_as_float(b4.w & 0xFFFF0000u)}; }
;                     const f32x4 o0 = b0 + acc[ai][bj][m][0], o1 = b1 + acc[ai][bj][m][1];
;                     if (out32) {
;                         if (!dry) { *(f32x4*)(out32 + off + bj * HALF) = o0; *(f32x4*)(out32 + off + bj * HALF + 4) = o1; }
.LBB0_2185:
	s_waitcnt vmcnt(14)
	v_lshlrev_b32_e32 v158, 16, v186
	v_and_b32_e32 v159, 0xffff0000, v186
	v_lshlrev_b32_e32 v160, 16, v187
	v_and_b32_e32 v161, 0xffff0000, v187
	v_lshlrev_b32_e32 v162, 16, v188
	v_and_b32_e32 v163, 0xffff0000, v188
	v_lshlrev_b32_e32 v164, 16, v189
	v_and_b32_e32 v165, 0xffff0000, v189
	v_pk_add_f32 v[152:153], v[152:153], v[160:161]
	v_pk_add_f32 v[150:151], v[150:151], v[158:159]
	v_pk_add_f32 v[144:145], v[144:145], v[164:165]
	v_pk_add_f32 v[142:143], v[142:143], v[162:163]
	s_and_b64 vcc, exec, s[10:11]
	s_mov_b64 s[12:13], -1
	s_cbranch_vccnz .LBB0_2187
	s_mov_b64 s[12:13], 0
	global_store_dwordx4 v[214:215], v[150:153], off offset:512
	global_store_dwordx4 v[214:215], v[142:145], off offset:528

;     __device__ __forceinline__ void operator()(const Acc& acc, const Unit& u, int wr, int wc, int fr, int fq, const LAS float* tab) const {
;     ...
;                     else { const u32x4 b4 = rb[ai][m][bj];
;                         b0 = (f32x4){__uint_as_float(b4.x << 16), __uint_as_float(b4.x & 0xFFFF0000u), __uint_as_float(b4.y << 16), __uint_as_float(b4.y & 0xFFFF0000u)};
;                         b1 = (f32x4){__uint_as_float(b4.z << 16), __uint_as_float(b4.z & 0xFFFF0000u), __uint_as_float(b4.w << 16), __uint_as_float(b4.w & 0xFFFF0000u)}; }
;                     const f32x4 o0 = b0 + acc[ai][bj][m][0], o1 = b1 + acc[ai][bj][m][1];
;                     if (out32) {
;                         if (!dry) { *(f32x4*)(out32 + off + bj * HALF) = o0; *(f32x4*)(out32 + off + bj * HALF + 4) = o1; }
.LBB0_2193:
	v_or_b32_e32 v142, 16, v210
	v_mov_b32_e32 v143, v211
	v_lshlrev_b64 v[144:145], 10, v[142:143]
	v_lshl_add_u64 v[144:145], v[144:145], 0, v[208:209]
	s_waitcnt vmcnt(13)
	v_lshlrev_b32_e32 v150, 16, v182
	v_and_b32_e32 v151, 0xffff0000, v182
	v_lshlrev_b32_e32 v152, 16, v183
	v_and_b32_e32 v153, 0xffff0000, v183
	v_lshlrev_b32_e32 v158, 16, v184
	v_and_b32_e32 v159, 0xffff0000, v184
	v_lshlrev_b32_e32 v160, 16, v185
	v_and_b32_e32 v161, 0xffff0000, v185
	v_pk_add_f32 v[136:137], v[136:137], v[152:153]
	v_pk_add_f32 v[134:135], v[134:135], v[150:151]
	v_pk_add_f32 v[132:133], v[132:133], v[160:161]
	v_pk_add_f32 v[130:131], v[130:131], v[158:159]
	s_mov_b64 s[36:37], -1
	s_and_b64 vcc, exec, s[10:11]
	v_lshl_add_u64 v[150:151], v[144:145], 2, s[18:19]
	s_cbranch_vccnz .LBB0_2195
	s_mov_b64 s[36:37], 0
	global_store_dwordx4 v[150:151], v[134:137], off
	global_store_dwordx4 v[150:151], v[130:133], off offset:16

;     __device__ __forceinline__ void operator()(const Acc& acc, const Unit& u, int wr, int wc, int fr, int fq, const LAS float* tab) const {
;     ...
;                 const size_t row = (size_t)u.pm * BM + ai * HALF + wr * 64 + m * 16 + fr; const size_t off = row * D + col0; float ss = 0.f;
; #pragma unroll
;                 for (int bj = 0; bj < 2; ++bj) { f32x4 b0, b1;
;                     if (base32) { b0 = __builtin_nontemporal_load((const f32x4*)(base32 + off + bj * HALF)); b1 = __builtin_nontemporal_load((const f32x4*)(base32 + off + bj * HALF + 4)); }
;                     else { const u32x4 b4 = rb[ai][m][bj];
;                         b0 = (f32x4){__uint_as_float(b4.x << 16), __uint_as_float(b4.x & 0xFFFF0000u), __uint_as_float(b4.y << 16), __uint_as_float(b4.y & 0xFFFF0000u)};
;                         b1 = (f32x4){__uint_as_float(b4.z << 16), __uint_as_float(b4.z & 0xFFFF0000u), __uint_as_float(b4.w << 16), __uint_as_float(b4.w & 0xFFFF0000u)}; }
;                     const f32x4 o0 = b0 + acc[ai][bj][m][0], o1 = b1 + acc[ai][bj][m][1];
;                     if (out32) {
;                         if (!dry) { *(f32x4*)(out32 + off + bj * HALF) = o0; *(f32x4*)(out32 + off + bj * HALF + 4) = o1; }
.LBB0_2197:
	s_waitcnt vmcnt(12)
	v_lshlrev_b32_e32 v130, 16, v178
	v_and_b32_e32 v131, 0xffff0000, v178
	v_lshlrev_b32_e32 v132, 16, v179
	v_and_b32_e32 v133, 0xffff0000, v179
	v_lshlrev_b32_e32 v134, 16, v180
	v_and_b32_e32 v135, 0xffff0000, v180
	v_lshlrev_b32_e32 v136, 16, v181
	v_and_b32_e32 v137, 0xffff0000, v181
	v_pk_add_f32 v[124:125], v[124:125], v[132:133]
	v_pk_add_f32 v[122:123], v[122:123], v[130:131]
	v_pk_add_f32 v[120:121], v[120:121], v[136:137]
	v_pk_add_f32 v[118:119], v[118:119], v[134:135]
	s_and_b64 vcc, exec, s[10:11]
	s_mov_b64 s[36:37], -1
	s_cbranch_vccnz .LBB0_2200
	global_store_dwordx4 v[150:151], v[122:125], off offset:512
	global_store_dwordx4 v[150:151], v[118:121], off offset:528
	s_cbranch_execz .LBB0_2201

;     __device__ __forceinline__ void operator()(const Acc& acc, const Unit& u, int wr, int wc, int fr, int fq, const LAS float* tab) const {
;     ...
;                 const size_t row = (size_t)u.pm * BM + ai * HALF + wr * 64 + m * 16 + fr; const size_t off = row * D + col0; float ss = 0.f;
; #pragma unroll
;                 for (int bj = 0; bj < 2; ++bj) { f32x4 b0, b1;
;                     if (base32) { b0 = __builtin_nontemporal_load((const f32x4*)(base32 + off + bj * HALF)); b1 = __builtin_nontemporal_load((const f32x4*)(base32 + off + bj * HALF + 4)); }
;                     else { const u32x4 b4 = rb[ai][m][bj];
;                         b0 = (f32x4){__uint_as_float(b4.x << 16), __uint_as_float(b4.x & 0xFFFF0000u), __uint_as_float(b4.y << 16), __uint_as_float(b4.y & 0xFFFF0000u)};
;                         b1 = (f32x4){__uint_as_float(b4.z << 16), __uint_as_float(b4.z & 0xFFFF0000u), __uint_as_float(b4.w << 16), __uint_as_float(b4.w & 0xFFFF0000u)}; }
;                     const f32x4 o0 = b0 + acc[ai][bj][m][0], o1 = b1 + acc[ai][bj][m][1];
;                     if (out32) {
;                         if (!dry) { *(f32x4*)(out32 + off + bj * HALF) = o0; *(f32x4*)(out32 + off + bj * HALF + 4) = o1; }
.LBB0_2205:
	v_or_b32_e32 v118, 32, v210
	v_mov_b32_e32 v119, v211
	v_lshlrev_b64 v[120:121], 10, v[118:119]
	v_lshl_add_u64 v[120:121], v[120:121], 0, v[208:209]
	s_waitcnt vmcnt(11)
	v_lshlrev_b32_e32 v122, 16, v174
	v_and_b32_e32 v123, 0xffff0000, v174
	v_lshlrev_b32_e32 v124, 16, v175
	v_and_b32_e32 v125, 0xffff0000, v175
	v_lshlrev_b32_e32 v130, 16, v176
	v_and_b32_e32 v131, 0xffff0000, v176
	v_lshlrev_b32_e32 v132, 16, v177
	v_and_b32_e32 v133, 0xffff0000, v177
	v_pk_add_f32 v[112:113], v[112:113], v[124:125]
	v_pk_add_f32 v[110:111], v[110:111], v[122:123]
	v_pk_add_f32 v[108:109], v[108:109], v[132:133]
	v_pk_add_f32 v[106:107], v[106:107], v[130:131]
	s_mov_b64 s[36:37], -1
	s_and_b64 vcc, exec, s[10:11]
	v_lshl_add_u64 v[122:123], v[120:121], 2, s[18:19]
	s_cbranch_vccnz .LBB0_2207
	s_mov_b64 s[36:37], 0
	global_store_dwordx4 v[122:123], v[110:113], off
	global_store_dwordx4 v[122:123], v[106:109], off offset:16

;     __device__ __forceinline__ void operator()(const Acc& acc, const Unit& u, int wr, int wc, int fr, int fq, const LAS float* tab) const {
;     ...
;                 const size_t row = (size_t)u.pm * BM + ai * HALF + wr * 64 + m * 16 + fr; const size_t off = row * D + col0; float ss = 0.f;
; #pragma unroll
;                 for (int bj = 0; bj < 2; ++bj) { f32x4 b0, b1;
;                     if (base32) { b0 = __builtin_nontemporal_load((const f32x4*)(base32 + off + bj * HALF)); b1 = __builtin_nontemporal_load((const f32x4*)(base32 + off + bj * HALF + 4)); }
;                     else { const u32x4 b4 = rb[ai][m][bj];
;                         b0 = (f32x4){__uint_as_float(b4.x << 16), __uint_as_float(b4.x & 0xFFFF0000u), __uint_as_float(b4.y << 16), __uint_as_float(b4.y & 0xFFFF0000u)};
;                         b1 = (f32x4){__uint_as_float(b4.z << 16), __uint_as_float(b4.z & 0xFFFF0000u), __uint_as_float(b4.w << 16), __uint_as_float(b4.w & 0xFFFF0000u)}; }
;                     const f32x4 o0 = b0 + acc[ai][bj][m][0], o1 = b1 + acc[ai][bj][m][1];
;                     if (out32) {
;                         if (!dry) { *(f32x4*)(out32 + off + bj * HALF) = o0; *(f32x4*)(out32 + off + bj * HALF + 4) = o1; }
.LBB0_2209:
	s_waitcnt vmcnt(10)
	v_lshlrev_b32_e32 v106, 16, v170
	v_and_b32_e32 v107, 0xffff0000, v170
	v_lshlrev_b32_e32 v108, 16, v171
	v_and_b32_e32 v109, 0xffff0000, v171
	v_lshlrev_b32_e32 v110, 16, v172
	v_and_b32_e32 v111, 0xffff0000, v172
	v_lshlrev_b32_e32 v112, 16, v173
	v_and_b32_e32 v113, 0xffff0000, v173
	v_pk_add_f32 v[100:101], v[100:101], v[108:109]
	v_pk_add_f32 v[98:99], v[98:99], v[106:107]
	v_pk_add_f32 v[96:97], v[96:97], v[112:113]
	v_pk_add_f32 v[94:95], v[94:95], v[110:111]
	s_and_b64 vcc, exec, s[10:11]
	s_mov_b64 s[36:37], -1
	s_cbranch_vccnz .LBB0_2212
	global_store_dwordx4 v[122:123], v[98:101], off offset:512
	global_store_dwordx4 v[122:123], v[94:97], off offset:528
	s_cbranch_execz .LBB0_2213

;     __device__ __forceinline__ void operator()(const Acc& acc, const Unit& u, int wr, int wc, int fr, int fq, const LAS float* tab) const {
;     ...
;                 const size_t row = (size_t)u.pm * BM + ai * HALF + wr * 64 + m * 16 + fr; const size_t off = row * D + col0; float ss = 0.f;
; #pragma unroll
;                 for (int bj = 0; bj < 2; ++bj) { f32x4 b0, b1;
;                     if (base32) { b0 = __builtin_nontemporal_load((const f32x4*)(base32 + off + bj * HALF)); b1 = __builtin_nontemporal_load((const f32x4*)(base32 + off + bj * HALF + 4)); }
;                     else { const u32x4 b4 = rb[ai][m][bj];
;                         b0 = (f32x4){__uint_as_float(b4.x << 16), __uint_as_float(b4.x & 0xFFFF0000u), __uint_as_float(b4.y << 16), __uint_as_float(b4.y & 0xFFFF0000u)};
;                         b1 = (f32x4){__uint_as_float(b4.z << 16), __uint_as_float(b4.z & 0xFFFF0000u), __uint_as_float(b4.w << 16), __uint_as_float(b4.w & 0xFFFF0000u)}; }
;                     const f32x4 o0 = b0 + acc[ai][bj][m][0], o1 = b1 + acc[ai][bj][m][1];
;                     if (out32) {
;                         if (!dry) { *(f32x4*)(out32 + off + bj * HALF) = o0; *(f32x4*)(out32 + off + bj * HALF + 4) = o1; }
.LBB0_2217:
	v_or_b32_e32 v94, 48, v210
	v_mov_b32_e32 v95, v211
	v_lshlrev_b64 v[96:97], 10, v[94:95]
	v_lshl_add_u64 v[96:97], v[96:97], 0, v[208:209]
	s_waitcnt vmcnt(9)
	v_lshlrev_b32_e32 v98, 16, v166
	v_and_b32_e32 v99, 0xffff0000, v166
	v_lshlrev_b32_e32 v100, 16, v167
	v_and_b32_e32 v101, 0xffff0000, v167
	v_lshlrev_b32_e32 v106, 16, v168
	v_and_b32_e32 v107, 0xffff0000, v168
	v_lshlrev_b32_e32 v108, 16, v169
	v_and_b32_e32 v109, 0xffff0000, v169
	v_pk_add_f32 v[88:89], v[88:89], v[100:101]
	v_pk_add_f32 v[86:87], v[86:87], v[98:99]
	v_pk_add_f32 v[84:85], v[84:85], v[108:109]
	v_pk_add_f32 v[82:83], v[82:83], v[106:107]
	s_mov_b64 s[36:37], -1
	s_and_b64 vcc, exec, s[10:11]
	v_lshl_add_u64 v[98:99], v[96:97], 2, s[18:19]
	s_cbranch_vccnz .LBB0_2219
	s_mov_b64 s[36:37], 0
	global_store_dwordx4 v[98:99], v[86:89], off
	global_store_dwordx4 v[98:99], v[82:85], off offset:16

;     __device__ __forceinline__ void operator()(const Acc& acc, const Unit& u, int wr, int wc, int fr, int fq, const LAS float* tab) const {
;     ...
;                 const size_t row = (size_t)u.pm * BM + ai * HALF + wr * 64 + m * 16 + fr; const size_t off = row * D + col0; float ss = 0.f;
; #pragma unroll
;                 for (int bj = 0; bj < 2; ++bj) { f32x4 b0, b1;
;                     if (base32) { b0 = __builtin_nontemporal_load((const f32x4*)(base32 + off + bj * HALF)); b1 = __builtin_nontemporal_load((const f32x4*)(base32 + off + bj * HALF + 4)); }
;                     else { const u32x4 b4 = rb[ai][m][bj];
;                         b0 = (f32x4){__uint_as_float(b4.x << 16), __uint_as_float(b4.x & 0xFFFF0000u), __uint_as_float(b4.y << 16), __uint_as_float(b4.y & 0xFFFF0000u)};
;                         b1 = (f32x4){__uint_as_float(b4.z << 16), __uint_as_float(b4.z & 0xFFFF0000u), __uint_as_float(b4.w << 16), __uint_as_float(b4.w & 0xFFFF0000u)}; }
;                     const f32x4 o0 = b0 + acc[ai][bj][m][0], o1 = b1 + acc[ai][bj][m][1];
;                     if (out32) {
;                         if (!dry) { *(f32x4*)(out32 + off + bj * HALF) = o0; *(f32x4*)(out32 + off + bj * HALF + 4) = o1; }
.LBB0_2221:
	s_waitcnt vmcnt(8)
	v_lshlrev_b32_e32 v82, 16, v154
	v_and_b32_e32 v83, 0xffff0000, v154
	v_lshlrev_b32_e32 v84, 16, v155
	v_and_b32_e32 v85, 0xffff0000, v155
	v_lshlrev_b32_e32 v86, 16, v156
	v_and_b32_e32 v87, 0xffff0000, v156
	v_lshlrev_b32_e32 v88, 16, v157
	v_and_b32_e32 v89, 0xffff0000, v157
	v_pk_add_f32 v[76:77], v[76:77], v[84:85]
	v_pk_add_f32 v[74:75], v[74:75], v[82:83]
	v_pk_add_f32 v[72:73], v[72:73], v[88:89]
	v_pk_add_f32 v[70:71], v[70:71], v[86:87]
	s_and_b64 vcc, exec, s[10:11]
	s_mov_b64 s[36:37], -1
	s_cbranch_vccnz .LBB0_2224
	global_store_dwordx4 v[98:99], v[74:77], off offset:512
	global_store_dwordx4 v[98:99], v[70:73], off offset:528
	s_cbranch_execz .LBB0_2225

;     __device__ __forceinline__ void operator()(const Acc& acc, const Unit& u, int wr, int wc, int fr, int fq, const LAS float* tab) const {
;     ...
;                 const size_t row = (size_t)u.pm * BM + ai * HALF + wr * 64 + m * 16 + fr; const size_t off = row * D + col0; float ss = 0.f;
; #pragma unroll
;                 for (int bj = 0; bj < 2; ++bj) { f32x4 b0, b1;
;                     if (base32) { b0 = __builtin_nontemporal_load((const f32x4*)(base32 + off + bj * HALF)); b1 = __builtin_nontemporal_load((const f32x4*)(base32 + off + bj * HALF + 4)); }
;                     else { const u32x4 b4 = rb[ai][m][bj];
;                         b0 = (f32x4){__uint_as_float(b4.x << 16), __uint_as_float(b4.x & 0xFFFF0000u), __uint_as_float(b4.y << 16), __uint_as_float(b4.y & 0xFFFF0000u)};
;                         b1 = (f32x4){__uint_as_float(b4.z << 16), __uint_as_float(b4.z & 0xFFFF0000u), __uint_as_float(b4.w << 16), __uint_as_float(b4.w & 0xFFFF0000u)}; }
;                     const f32x4 o0 = b0 + acc[ai][bj][m][0], o1 = b1 + acc[ai][bj][m][1];
;                     if (out32) {
;                         if (!dry) { *(f32x4*)(out32 + off + bj * HALF) = o0; *(f32x4*)(out32 + off + bj * HALF + 4) = o1; }
.LBB0_2229:
	v_lshl_add_u64 v[70:71], v[210:211], 0, s[90:91]
	v_lshlrev_b64 v[72:73], 10, v[70:71]
	v_lshl_add_u64 v[72:73], v[72:73], 0, v[208:209]
	s_waitcnt vmcnt(7)
	v_lshlrev_b32_e32 v74, 16, v146
	v_and_b32_e32 v75, 0xffff0000, v146
	v_lshlrev_b32_e32 v76, 16, v147
	v_and_b32_e32 v77, 0xffff0000, v147
	v_lshlrev_b32_e32 v82, 16, v148
	v_and_b32_e32 v83, 0xffff0000, v148
	v_lshlrev_b32_e32 v84, 16, v149
	v_and_b32_e32 v85, 0xffff0000, v149
	v_pk_add_f32 v[64:65], v[64:65], v[76:77]
	v_pk_add_f32 v[62:63], v[62:63], v[74:75]
	v_pk_add_f32 v[60:61], v[60:61], v[84:85]
	v_pk_add_f32 v[58:59], v[58:59], v[82:83]
	s_mov_b64 s[36:37], -1
	s_and_b64 vcc, exec, s[10:11]
	v_lshl_add_u64 v[74:75], v[72:73], 2, s[18:19]
	s_cbranch_vccnz .LBB0_2231
	s_mov_b64 s[36:37], 0
	global_store_dwordx4 v[74:75], v[62:65], off
	global_store_dwordx4 v[74:75], v[58:61], off offset:16

;     __device__ __forceinline__ void operator()(const Acc& acc, const Unit& u, int wr, int wc, int fr, int fq, const LAS float* tab) const {
;     ...
;                 const size_t row = (size_t)u.pm * BM + ai * HALF + wr * 64 + m * 16 + fr; const size_t off = row * D + col0; float ss = 0.f;
; #pragma unroll
;                 for (int bj = 0; bj < 2; ++bj) { f32x4 b0, b1;
;                     if (base32) { b0 = __builtin_nontemporal_load((const f32x4*)(base32 + off + bj * HALF)); b1 = __builtin_nontemporal_load((const f32x4*)(base32 + off + bj * HALF + 4)); }
;                     else { const u32x4 b4 = rb[ai][m][bj];
;                         b0 = (f32x4){__uint_as_float(b4.x << 16), __uint_as_float(b4.x & 0xFFFF0000u), __uint_as_float(b4.y << 16), __uint_as_float(b4.y & 0xFFFF0000u)};
;                         b1 = (f32x4){__uint_as_float(b4.z << 16), __uint_as_float(b4.z & 0xFFFF0000u), __uint_as_float(b4.w << 16), __uint_as_float(b4.w & 0xFFFF0000u)}; }
;                     const f32x4 o0 = b0 + acc[ai][bj][m][0], o1 = b1 + acc[ai][bj][m][1];
;                     if (out32) {
;                         if (!dry) { *(f32x4*)(out32 + off + bj * HALF) = o0; *(f32x4*)(out32 + off + bj * HALF + 4) = o1; }
.LBB0_2233:
	s_waitcnt vmcnt(6)
	v_lshlrev_b32_e32 v58, 16, v138
	v_and_b32_e32 v59, 0xffff0000, v138
	v_lshlrev_b32_e32 v60, 16, v139
	v_and_b32_e32 v61, 0xffff0000, v139
	v_lshlrev_b32_e32 v62, 16, v140
	v_and_b32_e32 v63, 0xffff0000, v140
	v_lshlrev_b32_e32 v64, 16, v141
	v_and_b32_e32 v65, 0xffff0000, v141
	v_pk_add_f32 v[56:57], v[56:57], v[60:61]
	v_pk_add_f32 v[54:55], v[54:55], v[58:59]
	v_pk_add_f32 v[52:53], v[52:53], v[64:65]
	v_pk_add_f32 v[50:51], v[50:51], v[62:63]
	s_and_b64 vcc, exec, s[10:11]
	s_mov_b64 s[36:37], -1
	s_cbranch_vccnz .LBB0_2236
	global_store_dwordx4 v[74:75], v[54:57], off offset:512
	global_store_dwordx4 v[74:75], v[50:53], off offset:528
	s_cbranch_execz .LBB0_2237

;     __device__ __forceinline__ void operator()(const Acc& acc, const Unit& u, int wr, int wc, int fr, int fq, const LAS float* tab) const {
;     ...
;                 const size_t row = (size_t)u.pm * BM + ai * HALF + wr * 64 + m * 16 + fr; const size_t off = row * D + col0; float ss = 0.f;
; #pragma unroll
;                 for (int bj = 0; bj < 2; ++bj) { f32x4 b0, b1;
;                     if (base32) { b0 = __builtin_nontemporal_load((const f32x4*)(base32 + off + bj * HALF)); b1 = __builtin_nontemporal_load((const f32x4*)(base32 + off + bj * HALF + 4)); }
;                     else { const u32x4 b4 = rb[ai][m][bj];
;                         b0 = (f32x4){__uint_as_float(b4.x << 16), __uint_as_float(b4.x & 0xFFFF0000u), __uint_as_float(b4.y << 16), __uint_as_float(b4.y & 0xFFFF0000u)};
;                         b1 = (f32x4){__uint_as_float(b4.z << 16), __uint_as_float(b4.z & 0xFFFF0000u), __uint_as_float(b4.w << 16), __uint_as_float(b4.w & 0xFFFF0000u)}; }
;                     const f32x4 o0 = b0 + acc[ai][bj][m][0], o1 = b1 + acc[ai][bj][m][1];
;                     if (out32) {
;                         if (!dry) { *(f32x4*)(out32 + off + bj * HALF) = o0; *(f32x4*)(out32 + off + bj * HALF + 4) = o1; }
.LBB0_2241:
	s_mov_b64 s[0:1], 0x90
	v_lshl_add_u64 v[50:51], v[210:211], 0, s[0:1]
	v_lshlrev_b64 v[52:53], 10, v[50:51]
	v_lshl_add_u64 v[52:53], v[52:53], 0, v[208:209]
	s_waitcnt vmcnt(5)
	v_lshlrev_b32_e32 v54, 16, v126
	v_and_b32_e32 v55, 0xffff0000, v126
	v_lshlrev_b32_e32 v56, 16, v127
	v_and_b32_e32 v57, 0xffff0000, v127
	v_lshlrev_b32_e32 v58, 16, v128
	v_and_b32_e32 v59, 0xffff0000, v128
	v_lshlrev_b32_e32 v60, 16, v129
	v_and_b32_e32 v61, 0xffff0000, v129
	v_pk_add_f32 v[48:49], v[48:49], v[56:57]
	v_pk_add_f32 v[46:47], v[46:47], v[54:55]
	v_pk_add_f32 v[44:45], v[44:45], v[60:61]
	v_pk_add_f32 v[42:43], v[42:43], v[58:59]
	s_mov_b64 s[36:37], -1
	s_and_b64 vcc, exec, s[10:11]
	v_lshl_add_u64 v[54:55], v[52:53], 2, s[18:19]
	s_cbranch_vccnz .LBB0_2243
	s_mov_b64 s[36:37], 0
	global_store_dwordx4 v[54:55], v[46:49], off
	global_store_dwordx4 v[54:55], v[42:45], off offset:16

;     __device__ __forceinline__ void operator()(const Acc& acc, const Unit& u, int wr, int wc, int fr, int fq, const LAS float* tab) const {
;     ...
;                 const size_t row = (size_t)u.pm * BM + ai * HALF + wr * 64 + m * 16 + fr; const size_t off = row * D + col0; float ss = 0.f;
; #pragma unroll
;                 for (int bj = 0; bj < 2; ++bj) { f32x4 b0, b1;
;                     if (base32) { b0 = __builtin_nontemporal_load((const f32x4*)(base32 + off + bj * HALF)); b1 = __builtin_nontemporal_load((const f32x4*)(base32 + off + bj * HALF + 4)); }
;                     else { const u32x4 b4 = rb[ai][m][bj];
;                         b0 = (f32x4){__uint_as_float(b4.x << 16), __uint_as_float(b4.x & 0xFFFF0000u), __uint_as_float(b4.y << 16), __uint_as_float(b4.y & 0xFFFF0000u)};
;                         b1 = (f32x4){__uint_as_float(b4.z << 16), __uint_as_float(b4.z & 0xFFFF0000u), __uint_as_float(b4.w << 16), __uint_as_float(b4.w & 0xFFFF0000u)}; }
;                     const f32x4 o0 = b0 + acc[ai][bj][m][0], o1 = b1 + acc[ai][bj][m][1];
;                     if (out32) {
;                         if (!dry) { *(f32x4*)(out32 + off + bj * HALF) = o0; *(f32x4*)(out32 + off + bj * HALF + 4) = o1; }
.LBB0_2245:
	s_waitcnt vmcnt(4)
	v_lshlrev_b32_e32 v42, 16, v114
	v_and_b32_e32 v43, 0xffff0000, v114
	v_lshlrev_b32_e32 v44, 16, v115
	v_and_b32_e32 v45, 0xffff0000, v115
	v_lshlrev_b32_e32 v46, 16, v116
	v_and_b32_e32 v47, 0xffff0000, v116
	v_lshlrev_b32_e32 v48, 16, v117
	v_and_b32_e32 v49, 0xffff0000, v117
	v_pk_add_f32 v[40:41], v[40:41], v[44:45]
	v_pk_add_f32 v[38:39], v[38:39], v[42:43]
	v_pk_add_f32 v[36:37], v[36:37], v[48:49]
	v_pk_add_f32 v[34:35], v[34:35], v[46:47]
	s_and_b64 vcc, exec, s[10:11]
	s_mov_b64 s[36:37], -1
	s_cbranch_vccnz .LBB0_2248
	global_store_dwordx4 v[54:55], v[38:41], off offset:512
	global_store_dwordx4 v[54:55], v[34:37], off offset:528
	s_cbranch_execz .LBB0_2249

;     __device__ __forceinline__ void operator()(const Acc& acc, const Unit& u, int wr, int wc, int fr, int fq, const LAS float* tab) const {
;     ...
;                 const size_t row = (size_t)u.pm * BM + ai * HALF + wr * 64 + m * 16 + fr; const size_t off = row * D + col0; float ss = 0.f;
; #pragma unroll
;                 for (int bj = 0; bj < 2; ++bj) { f32x4 b0, b1;
;                     if (base32) { b0 = __builtin_nontemporal_load((const f32x4*)(base32 + off + bj * HALF)); b1 = __builtin_nontemporal_load((const f32x4*)(base32 + off + bj * HALF + 4)); }
;                     else { const u32x4 b4 = rb[ai][m][bj];
;                         b0 = (f32x4){__uint_as_float(b4.x << 16), __uint_as_float(b4.x & 0xFFFF0000u), __uint_as_float(b4.y << 16), __uint_as_float(b4.y & 0xFFFF0000u)};
;                         b1 = (f32x4){__uint_as_float(b4.z << 16), __uint_as_float(b4.z & 0xFFFF0000u), __uint_as_float(b4.w << 16), __uint_as_float(b4.w & 0xFFFF0000u)}; }
;                     const f32x4 o0 = b0 + acc[ai][bj][m][0], o1 = b1 + acc[ai][bj][m][1];
;                     if (out32) {
;                         if (!dry) { *(f32x4*)(out32 + off + bj * HALF) = o0; *(f32x4*)(out32 + off + bj * HALF + 4) = o1; }
.LBB0_2253:
	s_mov_b64 s[0:1], 0xa0
	v_lshl_add_u64 v[34:35], v[210:211], 0, s[0:1]
	v_lshlrev_b64 v[36:37], 10, v[34:35]
	v_lshl_add_u64 v[36:37], v[36:37], 0, v[208:209]
	s_waitcnt vmcnt(3)
	v_lshlrev_b32_e32 v38, 16, v102
	v_and_b32_e32 v39, 0xffff0000, v102
	v_lshlrev_b32_e32 v40, 16, v103
	v_and_b32_e32 v41, 0xffff0000, v103
	v_lshlrev_b32_e32 v42, 16, v104
	v_and_b32_e32 v43, 0xffff0000, v104
	v_lshlrev_b32_e32 v44, 16, v105
	v_and_b32_e32 v45, 0xffff0000, v105
	v_pk_add_f32 v[32:33], v[32:33], v[40:41]
	v_pk_add_f32 v[30:31], v[30:31], v[38:39]
	v_pk_add_f32 v[28:29], v[28:29], v[44:45]
	v_pk_add_f32 v[26:27], v[26:27], v[42:43]
	s_mov_b64 s[36:37], -1
	s_and_b64 vcc, exec, s[10:11]
	v_lshl_add_u64 v[38:39], v[36:37], 2, s[18:19]
	s_cbranch_vccnz .LBB0_2255
	s_mov_b64 s[36:37], 0
	global_store_dwordx4 v[38:39], v[30:33], off
	global_store_dwordx4 v[38:39], v[26:29], off offset:16

;     __device__ __forceinline__ void operator()(const Acc& acc, const Unit& u, int wr, int wc, int fr, int fq, const LAS float* tab) const {
;     ...
;                 const size_t row = (size_t)u.pm * BM + ai * HALF + wr * 64 + m * 16 + fr; const size_t off = row * D + col0; float ss = 0.f;
; #pragma unroll
;                 for (int bj = 0; bj < 2; ++bj) { f32x4 b0, b1;
;                     if (base32) { b0 = __builtin_nontemporal_load((const f32x4*)(base32 + off + bj * HALF)); b1 = __builtin_nontemporal_load((const f32x4*)(base32 + off + bj * HALF + 4)); }
;                     else { const u32x4 b4 = rb[ai][m][bj];
;                         b0 = (f32x4){__uint_as_float(b4.x << 16), __uint_as_float(b4.x & 0xFFFF0000u), __uint_as_float(b4.y << 16), __uint_as_float(b4.y & 0xFFFF0000u)};
;                         b1 = (f32x4){__uint_as_float(b4.z << 16), __uint_as_float(b4.z & 0xFFFF0000u), __uint_as_float(b4.w << 16), __uint_as_float(b4.w & 0xFFFF0000u)}; }
;                     const f32x4 o0 = b0 + acc[ai][bj][m][0], o1 = b1 + acc[ai][bj][m][1];
;                     if (out32) {
;                         if (!dry) { *(f32x4*)(out32 + off + bj * HALF) = o0; *(f32x4*)(out32 + off + bj * HALF + 4) = o1; }
.LBB0_2257:
	s_waitcnt vmcnt(2)
	v_lshlrev_b32_e32 v26, 16, v90
	v_and_b32_e32 v27, 0xffff0000, v90
	v_lshlrev_b32_e32 v28, 16, v91
	v_and_b32_e32 v29, 0xffff0000, v91
	v_lshlrev_b32_e32 v30, 16, v92
	v_and_b32_e32 v31, 0xffff0000, v92
	v_lshlrev_b32_e32 v32, 16, v93
	v_and_b32_e32 v33, 0xffff0000, v93
	v_pk_add_f32 v[24:25], v[24:25], v[28:29]
	v_pk_add_f32 v[22:23], v[22:23], v[26:27]
	v_pk_add_f32 v[20:21], v[20:21], v[32:33]
	v_pk_add_f32 v[18:19], v[18:19], v[30:31]
	s_and_b64 vcc, exec, s[10:11]
	s_mov_b64 s[36:37], -1
	s_cbranch_vccnz .LBB0_2260
	global_store_dwordx4 v[38:39], v[22:25], off offset:512
	global_store_dwordx4 v[38:39], v[18:21], off offset:528
	s_cbranch_execz .LBB0_2261

;     __device__ __forceinline__ void operator()(const Acc& acc, const Unit& u, int wr, int wc, int fr, int fq, const LAS float* tab) const {
;     ...
;                 const size_t row = (size_t)u.pm * BM + ai * HALF + wr * 64 + m * 16 + fr; const size_t off = row * D + col0; float ss = 0.f;
; #pragma unroll
;                 for (int bj = 0; bj < 2; ++bj) { f32x4 b0, b1;
;                     if (base32) { b0 = __builtin_nontemporal_load((const f32x4*)(base32 + off + bj * HALF)); b1 = __builtin_nontemporal_load((const f32x4*)(base32 + off + bj * HALF + 4)); }
;                     else { const u32x4 b4 = rb[ai][m][bj];
;                         b0 = (f32x4){__uint_as_float(b4.x << 16), __uint_as_float(b4.x & 0xFFFF0000u), __uint_as_float(b4.y << 16), __uint_as_float(b4.y & 0xFFFF0000u)};
;                         b1 = (f32x4){__uint_as_float(b4.z << 16), __uint_as_float(b4.z & 0xFFFF0000u), __uint_as_float(b4.w << 16), __uint_as_float(b4.w & 0xFFFF0000u)}; }
;                     const f32x4 o0 = b0 + acc[ai][bj][m][0], o1 = b1 + acc[ai][bj][m][1];
;                     if (out32) {
;                         if (!dry) { *(f32x4*)(out32 + off + bj * HALF) = o0; *(f32x4*)(out32 + off + bj * HALF + 4) = o1; }
.LBB0_2265:
	s_mov_b64 s[0:1], 0xb0
	v_lshl_add_u64 v[18:19], v[210:211], 0, s[0:1]
	v_lshlrev_b64 v[20:21], 10, v[18:19]
	v_lshl_add_u64 v[20:21], v[20:21], 0, v[208:209]
	s_waitcnt vmcnt(1)
	v_lshlrev_b32_e32 v22, 16, v78
	v_and_b32_e32 v23, 0xffff0000, v78
	v_lshlrev_b32_e32 v24, 16, v79
	v_and_b32_e32 v25, 0xffff0000, v79
	v_lshlrev_b32_e32 v26, 16, v80
	v_and_b32_e32 v27, 0xffff0000, v80
	v_lshlrev_b32_e32 v28, 16, v81
	v_and_b32_e32 v29, 0xffff0000, v81
	v_pk_add_f32 v[16:17], v[16:17], v[24:25]
	v_pk_add_f32 v[14:15], v[14:15], v[22:23]
	v_pk_add_f32 v[12:13], v[12:13], v[28:29]
	v_pk_add_f32 v[10:11], v[10:11], v[26:27]
	s_mov_b64 s[36:37], -1
	s_and_b64 vcc, exec, s[10:11]
	v_lshl_add_u64 v[22:23], v[20:21], 2, s[18:19]
	s_cbranch_vccnz .LBB0_2267
	s_mov_b64 s[36:37], 0
	global_store_dwordx4 v[22:23], v[14:17], off
	global_store_dwordx4 v[22:23], v[10:13], off offset:16

;     __device__ __forceinline__ void operator()(const Acc& acc, const Unit& u, int wr, int wc, int fr, int fq, const LAS float* tab) const {
;     ...
;                 const size_t row = (size_t)u.pm * BM + ai * HALF + wr * 64 + m * 16 + fr; const size_t off = row * D + col0; float ss = 0.f;
; #pragma unroll
;                 for (int bj = 0; bj < 2; ++bj) { f32x4 b0, b1;
;                     if (base32) { b0 = __builtin_nontemporal_load((const f32x4*)(base32 + off + bj * HALF)); b1 = __builtin_nontemporal_load((const f32x4*)(base32 + off + bj * HALF + 4)); }
;                     else { const u32x4 b4 = rb[ai][m][bj];
;                         b0 = (f32x4){__uint_as_float(b4.x << 16), __uint_as_float(b4.x & 0xFFFF0000u), __uint_as_float(b4.y << 16), __uint_as_float(b4.y & 0xFFFF0000u)};
;                         b1 = (f32x4){__uint_as_float(b4.z << 16), __uint_as_float(b4.z & 0xFFFF0000u), __uint_as_float(b4.w << 16), __uint_as_float(b4.w & 0xFFFF0000u)}; }
;                     const f32x4 o0 = b0 + acc[ai][bj][m][0], o1 = b1 + acc[ai][bj][m][1];
;                     if (out32) {
;                         if (!dry) { *(f32x4*)(out32 + off + bj * HALF) = o0; *(f32x4*)(out32 + off + bj * HALF + 4) = o1; }
.LBB0_2269:
	s_waitcnt vmcnt(0)
	v_lshlrev_b32_e32 v10, 16, v66
	v_and_b32_e32 v11, 0xffff0000, v66
	v_lshlrev_b32_e32 v12, 16, v67
	v_and_b32_e32 v13, 0xffff0000, v67
	v_lshlrev_b32_e32 v14, 16, v68
	v_and_b32_e32 v15, 0xffff0000, v68
	v_lshlrev_b32_e32 v16, 16, v69
	v_and_b32_e32 v17, 0xffff0000, v69
	v_pk_add_f32 v[8:9], v[8:9], v[12:13]
	v_pk_add_f32 v[6:7], v[6:7], v[10:11]
	v_pk_add_f32 v[4:5], v[4:5], v[16:17]
	v_pk_add_f32 v[2:3], v[2:3], v[14:15]
	s_and_b64 vcc, exec, s[10:11]
	s_mov_b64 s[10:11], -1
	s_cbranch_vccnz .LBB0_2273
	global_store_dwordx4 v[22:23], v[6:9], off offset:512
	global_store_dwordx4 v[22:23], v[2:5], off offset:528
	s_cbranch_execz .LBB0_2274
